# G1 forget-gate (logsig) epilogue: four independent pairs per piece computed stage-interleaved instead of serial s_nop-padded chains
# speedup vs baseline: 1.0048x; 1.0048x over previous
.LBB0_326:
	s_and_b64 vcc, exec, s[24:25]
	s_cbranch_vccz .LBB0_328
	s_branch .Lg1ls_fast
	v_subrev_u32_e32 v130, s2, v64
	v_ashrrev_i32_e32 v131, 31, v130
	v_lshl_add_u64 v[134:135], v[130:131], 2, s[10:11]
	global_load_dwordx4 v[138:141], v[134:135], off offset:16
	global_load_dwordx4 v[142:145], v[134:135], off
	global_load_dwordx4 v[130:133], v[134:135], off offset:528
	s_nop 0
	global_load_dwordx4 v[134:137], v[134:135], off offset:512
	v_ashrrev_i32_e32 v159, 31, v64
	v_mov_b32_e32 v158, v64
	s_mov_b32 s24, 0xbfb8aa3b
	v_lshlrev_b64 v[164:165], 1, v[158:159]
	v_pk_mul_f32 v[158:159], v[126:127], s[24:25] op_sel_hi:[1,0]
	v_mov_b64_e32 v[162:163], s[8:9]
	v_exp_f32_e32 v158, v158
	v_exp_f32_e32 v159, v159
	s_movk_i32 s17, 0x2400
	v_mad_i64_i32 v[160:161], s[2:3], v189, s17, v[162:163]
	v_lshl_add_u64 v[178:179], v[160:161], 0, v[164:165]
	v_pk_add_f32 v[160:161], v[158:159], 1.0 op_sel_hi:[1,0]
	s_mov_b32 s26, 0x3f317218
	v_rcp_f32_e32 v160, v160
	v_rcp_f32_e32 v161, v161
	s_waitcnt vmcnt(0)
	v_pk_add_f32 v[158:159], v[142:143], 1.0 op_sel_hi:[1,0] neg_lo:[1,0] neg_hi:[1,0]
	s_nop 0
	v_pk_fma_f32 v[160:161], v[160:161], v[158:159], v[142:143]
	s_nop 0
	v_max_f32_e32 v161, 0xda24260, v161
	v_max_f32_e32 v160, 0xda24260, v160
	v_log_f32_e32 v160, v160
	v_log_f32_e32 v161, v161
	s_nop 0
	v_pk_mul_f32 v[170:171], v[160:161], s[26:27] op_sel_hi:[1,0]
	v_pk_mul_f32 v[160:161], v[128:129], s[24:25] op_sel_hi:[1,0]
	v_cvt_pk_bf16_f32 v170, v170, v171
	s_nop 0
	v_exp_f32_e32 v160, v160
	v_exp_f32_e32 v161, v161
	s_nop 0
	v_pk_add_f32 v[166:167], v[160:161], 1.0 op_sel_hi:[1,0]
	s_nop 0
	v_rcp_f32_e32 v166, v166
	v_rcp_f32_e32 v167, v167
	v_pk_add_f32 v[160:161], v[144:145], 1.0 op_sel_hi:[1,0] neg_lo:[1,0] neg_hi:[1,0]
	s_nop 0
	v_pk_fma_f32 v[166:167], v[166:167], v[160:161], v[144:145]
	s_nop 0
	v_max_f32_e32 v167, 0xda24260, v167
	v_max_f32_e32 v166, 0xda24260, v166
	v_log_f32_e32 v166, v166
	v_log_f32_e32 v167, v167
	s_nop 0
	v_pk_mul_f32 v[172:173], v[166:167], s[26:27] op_sel_hi:[1,0]
	v_pk_mul_f32 v[166:167], v[122:123], s[24:25] op_sel_hi:[1,0]
	v_cvt_pk_bf16_f32 v171, v172, v173
	s_nop 0
	v_exp_f32_e32 v166, v166
	v_exp_f32_e32 v167, v167
	s_nop 0
	v_pk_add_f32 v[168:169], v[166:167], 1.0 op_sel_hi:[1,0]
	s_nop 0
	v_rcp_f32_e32 v168, v168
	v_rcp_f32_e32 v169, v169
	v_pk_add_f32 v[166:167], v[138:139], 1.0 op_sel_hi:[1,0] neg_lo:[1,0] neg_hi:[1,0]
	s_nop 0
	v_pk_fma_f32 v[168:169], v[168:169], v[166:167], v[138:139]
	s_nop 0
	v_max_f32_e32 v169, 0xda24260, v169
	v_max_f32_e32 v168, 0xda24260, v168
	v_log_f32_e32 v168, v168
	v_log_f32_e32 v169, v169
	s_nop 0
	v_pk_mul_f32 v[174:175], v[168:169], s[26:27] op_sel_hi:[1,0]
	v_pk_mul_f32 v[168:169], v[124:125], s[24:25] op_sel_hi:[1,0]
	v_cvt_pk_bf16_f32 v172, v174, v175
	s_nop 0
	v_exp_f32_e32 v168, v168
	v_exp_f32_e32 v169, v169
	s_nop 0
	v_pk_add_f32 v[176:177], v[168:169], 1.0 op_sel_hi:[1,0]
	s_nop 0
	v_rcp_f32_e32 v176, v176
	v_rcp_f32_e32 v177, v177
	v_pk_add_f32 v[168:169], v[140:141], 1.0 op_sel_hi:[1,0] neg_lo:[1,0] neg_hi:[1,0]
	s_nop 0
	v_pk_fma_f32 v[176:177], v[176:177], v[168:169], v[140:141]
	s_nop 0
	v_max_f32_e32 v177, 0xda24260, v177
	v_max_f32_e32 v176, 0xda24260, v176
	v_log_f32_e32 v176, v176
	v_log_f32_e32 v177, v177
	s_nop 0
	v_pk_mul_f32 v[176:177], v[176:177], s[26:27] op_sel_hi:[1,0]
	s_nop 0
	v_cvt_pk_bf16_f32 v173, v176, v177
	global_store_dwordx4 v[178:179], v[170:173], off
	v_pk_add_f32 v[176:177], v[130:131], 1.0 op_sel_hi:[1,0] neg_lo:[1,0] neg_hi:[1,0]
	s_nop 0
	v_pk_mul_f32 v[170:171], v[114:115], s[24:25] op_sel_hi:[1,0]
	s_nop 0
	v_exp_f32_e32 v170, v170
	v_exp_f32_e32 v171, v171
	s_nop 0
	v_pk_add_f32 v[172:173], v[170:171], 1.0 op_sel_hi:[1,0]
	s_nop 0
	v_rcp_f32_e32 v172, v172
	v_rcp_f32_e32 v173, v173
	v_pk_add_f32 v[170:171], v[134:135], 1.0 op_sel_hi:[1,0] neg_lo:[1,0] neg_hi:[1,0]
	s_nop 0
	v_pk_fma_f32 v[172:173], v[172:173], v[170:171], v[134:135]
	s_nop 0
	v_max_f32_e32 v173, 0xda24260, v173
	v_max_f32_e32 v172, 0xda24260, v172
	v_log_f32_e32 v172, v172
	v_log_f32_e32 v173, v173
	s_nop 0
	v_pk_mul_f32 v[180:181], v[172:173], s[26:27] op_sel_hi:[1,0]
	v_pk_mul_f32 v[172:173], v[116:117], s[24:25] op_sel_hi:[1,0]
	v_cvt_pk_bf16_f32 v180, v180, v181
	s_nop 0
	v_exp_f32_e32 v172, v172
	v_exp_f32_e32 v173, v173
	s_nop 0
	v_pk_add_f32 v[174:175], v[172:173], 1.0 op_sel_hi:[1,0]
	s_nop 0
	v_rcp_f32_e32 v174, v174
	v_rcp_f32_e32 v175, v175
	v_pk_add_f32 v[172:173], v[136:137], 1.0 op_sel_hi:[1,0] neg_lo:[1,0] neg_hi:[1,0]
	s_nop 0
	v_pk_fma_f32 v[174:175], v[174:175], v[172:173], v[136:137]
	s_nop 0
	v_max_f32_e32 v175, 0xda24260, v175
	v_max_f32_e32 v174, 0xda24260, v174
	v_log_f32_e32 v174, v174
	v_log_f32_e32 v175, v175
	s_nop 0
	v_pk_mul_f32 v[182:183], v[174:175], s[26:27] op_sel_hi:[1,0]
	v_pk_mul_f32 v[174:175], v[106:107], s[24:25] op_sel_hi:[1,0]
	v_cvt_pk_bf16_f32 v181, v182, v183
	s_nop 0
	v_exp_f32_e32 v174, v174
	v_exp_f32_e32 v175, v175
	s_nop 0
	v_pk_add_f32 v[174:175], v[174:175], 1.0 op_sel_hi:[1,0]
	s_nop 0
	v_rcp_f32_e32 v174, v174
	v_rcp_f32_e32 v175, v175
	s_nop 0
	v_pk_fma_f32 v[174:175], v[174:175], v[176:177], v[130:131]
	s_nop 0
	v_max_f32_e32 v175, 0xda24260, v175
	v_max_f32_e32 v174, 0xda24260, v174
	v_log_f32_e32 v174, v174
	v_log_f32_e32 v175, v175
	s_nop 0
	v_pk_mul_f32 v[190:191], v[174:175], s[26:27] op_sel_hi:[1,0]
	v_pk_mul_f32 v[174:175], v[108:109], s[24:25] op_sel_hi:[1,0]
	v_cvt_pk_bf16_f32 v182, v190, v191
	v_pk_mul_f32 v[190:191], v[110:111], s[24:25] op_sel_hi:[1,0]
	v_exp_f32_e32 v174, v174
	v_exp_f32_e32 v175, v175
	v_exp_f32_e32 v190, v190
	v_exp_f32_e32 v191, v191
	v_pk_add_f32 v[192:193], v[174:175], 1.0 op_sel_hi:[1,0]
	s_nop 0
	v_rcp_f32_e32 v192, v192
	v_rcp_f32_e32 v193, v193
	v_pk_add_f32 v[174:175], v[132:133], 1.0 op_sel_hi:[1,0] neg_lo:[1,0] neg_hi:[1,0]
	v_pk_add_f32 v[190:191], v[190:191], 1.0 op_sel_hi:[1,0]
	v_pk_fma_f32 v[192:193], v[192:193], v[174:175], v[132:133]
	s_nop 0
	v_max_f32_e32 v193, 0xda24260, v193
	v_max_f32_e32 v192, 0xda24260, v192
	v_log_f32_e32 v192, v192
	v_log_f32_e32 v193, v193
	v_rcp_f32_e32 v190, v190
	v_rcp_f32_e32 v191, v191
	v_pk_mul_f32 v[192:193], v[192:193], s[26:27] op_sel_hi:[1,0]
	s_nop 0
	v_cvt_pk_bf16_f32 v183, v192, v193
	global_store_dwordx4 v[178:179], v[180:183], off offset:256
	v_pk_mul_f32 v[192:193], v[112:113], s[24:25] op_sel_hi:[1,0]
	v_pk_fma_f32 v[190:191], v[190:191], v[166:167], v[138:139]
	v_pk_mul_f32 v[180:181], v[118:119], s[24:25] op_sel_hi:[1,0]
	v_pk_mul_f32 v[182:183], v[120:121], s[24:25] op_sel_hi:[1,0]
	v_exp_f32_e32 v180, v180
	v_exp_f32_e32 v181, v181
	v_exp_f32_e32 v182, v182
	v_exp_f32_e32 v183, v183
	v_exp_f32_e32 v192, v192
	v_exp_f32_e32 v193, v193
	v_pk_add_f32 v[180:181], v[180:181], 1.0 op_sel_hi:[1,0]
	v_pk_add_f32 v[182:183], v[182:183], 1.0 op_sel_hi:[1,0]
	v_rcp_f32_e32 v180, v180
	v_rcp_f32_e32 v181, v181
	v_rcp_f32_e32 v182, v182
	v_rcp_f32_e32 v183, v183
	v_pk_add_f32 v[192:193], v[192:193], 1.0 op_sel_hi:[1,0]
	v_pk_fma_f32 v[180:181], v[180:181], v[158:159], v[142:143]
	v_rcp_f32_e32 v192, v192
	v_rcp_f32_e32 v193, v193
	v_pk_fma_f32 v[182:183], v[182:183], v[160:161], v[144:145]
	v_max_f32_e32 v181, 0xda24260, v181
	v_max_f32_e32 v180, 0xda24260, v180
	v_max_f32_e32 v183, 0xda24260, v183
	v_max_f32_e32 v182, 0xda24260, v182
	v_pk_fma_f32 v[192:193], v[192:193], v[168:169], v[140:141]
	v_log_f32_e32 v180, v180
	v_log_f32_e32 v181, v181
	v_log_f32_e32 v182, v182
	v_log_f32_e32 v183, v183
	v_max_f32_e32 v191, 0xda24260, v191
	v_max_f32_e32 v190, 0xda24260, v190
	v_max_f32_e32 v193, 0xda24260, v193
	v_max_f32_e32 v192, 0xda24260, v192
	v_log_f32_e32 v190, v190
	v_log_f32_e32 v191, v191
	v_log_f32_e32 v192, v192
	v_log_f32_e32 v193, v193
	v_or_b32_e32 v178, 16, v189
	v_mad_i64_i32 v[178:179], s[2:3], v178, s17, v[162:163]
	v_pk_mul_f32 v[180:181], v[180:181], s[26:27] op_sel_hi:[1,0]
	v_pk_mul_f32 v[182:183], v[182:183], s[26:27] op_sel_hi:[1,0]
	v_lshl_add_u64 v[178:179], v[178:179], 0, v[164:165]
	v_pk_mul_f32 v[190:191], v[190:191], s[26:27] op_sel_hi:[1,0]
	v_pk_mul_f32 v[192:193], v[192:193], s[26:27] op_sel_hi:[1,0]
	v_cvt_pk_bf16_f32 v180, v180, v181
	v_cvt_pk_bf16_f32 v181, v182, v183
	v_cvt_pk_bf16_f32 v182, v190, v191
	v_pk_mul_f32 v[190:191], v[90:91], s[24:25] op_sel_hi:[1,0]
	v_cvt_pk_bf16_f32 v183, v192, v193
	global_store_dwordx4 v[178:179], v[180:183], off
	v_pk_mul_f32 v[192:193], v[92:93], s[24:25] op_sel_hi:[1,0]
	v_exp_f32_e32 v190, v190
	v_pk_mul_f32 v[180:181], v[98:99], s[24:25] op_sel_hi:[1,0]
	v_pk_mul_f32 v[182:183], v[100:101], s[24:25] op_sel_hi:[1,0]
	v_exp_f32_e32 v180, v180
	v_exp_f32_e32 v181, v181
	v_exp_f32_e32 v182, v182
	v_exp_f32_e32 v183, v183
	v_exp_f32_e32 v191, v191
	v_exp_f32_e32 v192, v192
	v_exp_f32_e32 v193, v193
	v_pk_add_f32 v[180:181], v[180:181], 1.0 op_sel_hi:[1,0]
	v_pk_add_f32 v[182:183], v[182:183], 1.0 op_sel_hi:[1,0]
	v_rcp_f32_e32 v180, v180
	v_rcp_f32_e32 v181, v181
	v_rcp_f32_e32 v182, v182
	v_rcp_f32_e32 v183, v183
	v_pk_add_f32 v[190:191], v[190:191], 1.0 op_sel_hi:[1,0]
	v_pk_add_f32 v[192:193], v[192:193], 1.0 op_sel_hi:[1,0]
	v_rcp_f32_e32 v190, v190
	v_rcp_f32_e32 v191, v191
	v_rcp_f32_e32 v192, v192
	v_rcp_f32_e32 v193, v193
	v_pk_fma_f32 v[180:181], v[180:181], v[170:171], v[134:135]
	v_pk_fma_f32 v[182:183], v[182:183], v[172:173], v[136:137]
	v_max_f32_e32 v181, 0xda24260, v181
	v_max_f32_e32 v180, 0xda24260, v180
	v_max_f32_e32 v183, 0xda24260, v183
	v_max_f32_e32 v182, 0xda24260, v182
	v_pk_fma_f32 v[190:191], v[190:191], v[176:177], v[130:131]
	v_pk_fma_f32 v[192:193], v[192:193], v[174:175], v[132:133]
	v_log_f32_e32 v180, v180
	v_log_f32_e32 v181, v181
	v_log_f32_e32 v182, v182
	v_log_f32_e32 v183, v183
	v_max_f32_e32 v191, 0xda24260, v191
	v_max_f32_e32 v190, 0xda24260, v190
	v_max_f32_e32 v193, 0xda24260, v193
	v_max_f32_e32 v192, 0xda24260, v192
	v_log_f32_e32 v190, v190
	v_log_f32_e32 v191, v191
	v_log_f32_e32 v192, v192
	v_log_f32_e32 v193, v193
	v_pk_mul_f32 v[180:181], v[180:181], s[26:27] op_sel_hi:[1,0]
	v_pk_mul_f32 v[182:183], v[182:183], s[26:27] op_sel_hi:[1,0]
	v_pk_mul_f32 v[190:191], v[190:191], s[26:27] op_sel_hi:[1,0]
	v_pk_mul_f32 v[192:193], v[192:193], s[26:27] op_sel_hi:[1,0]
	v_cvt_pk_bf16_f32 v180, v180, v181
	v_cvt_pk_bf16_f32 v181, v182, v183
	v_cvt_pk_bf16_f32 v182, v190, v191
	v_pk_mul_f32 v[190:191], v[94:95], s[24:25] op_sel_hi:[1,0]
	v_cvt_pk_bf16_f32 v183, v192, v193
	global_store_dwordx4 v[178:179], v[180:183], off offset:256
	v_pk_mul_f32 v[192:193], v[96:97], s[24:25] op_sel_hi:[1,0]
	v_exp_f32_e32 v190, v190
	v_pk_mul_f32 v[180:181], v[102:103], s[24:25] op_sel_hi:[1,0]
	v_pk_mul_f32 v[182:183], v[104:105], s[24:25] op_sel_hi:[1,0]
	v_exp_f32_e32 v180, v180
	v_exp_f32_e32 v181, v181
	v_exp_f32_e32 v182, v182
	v_exp_f32_e32 v183, v183
	v_exp_f32_e32 v191, v191
	v_exp_f32_e32 v192, v192
	v_exp_f32_e32 v193, v193
	v_pk_add_f32 v[180:181], v[180:181], 1.0 op_sel_hi:[1,0]
	v_pk_add_f32 v[182:183], v[182:183], 1.0 op_sel_hi:[1,0]
	v_rcp_f32_e32 v180, v180
	v_rcp_f32_e32 v181, v181
	v_rcp_f32_e32 v182, v182
	v_rcp_f32_e32 v183, v183
	v_pk_add_f32 v[190:191], v[190:191], 1.0 op_sel_hi:[1,0]
	v_pk_add_f32 v[192:193], v[192:193], 1.0 op_sel_hi:[1,0]
	v_rcp_f32_e32 v190, v190
	v_rcp_f32_e32 v191, v191
	v_rcp_f32_e32 v192, v192
	v_rcp_f32_e32 v193, v193
	v_pk_fma_f32 v[180:181], v[180:181], v[158:159], v[142:143]
	v_pk_fma_f32 v[182:183], v[182:183], v[160:161], v[144:145]
	v_max_f32_e32 v181, 0xda24260, v181
	v_max_f32_e32 v180, 0xda24260, v180
	v_max_f32_e32 v183, 0xda24260, v183
	v_max_f32_e32 v182, 0xda24260, v182
	v_pk_fma_f32 v[190:191], v[190:191], v[166:167], v[138:139]
	v_pk_fma_f32 v[192:193], v[192:193], v[168:169], v[140:141]
	v_log_f32_e32 v180, v180
	v_log_f32_e32 v181, v181
	v_log_f32_e32 v182, v182
	v_log_f32_e32 v183, v183
	v_max_f32_e32 v191, 0xda24260, v191
	v_max_f32_e32 v190, 0xda24260, v190
	v_max_f32_e32 v193, 0xda24260, v193
	v_max_f32_e32 v192, 0xda24260, v192
	v_log_f32_e32 v190, v190
	v_log_f32_e32 v191, v191
	v_log_f32_e32 v192, v192
	v_log_f32_e32 v193, v193
	v_or_b32_e32 v178, 32, v189
	v_mad_i64_i32 v[178:179], s[2:3], v178, s17, v[162:163]
	v_pk_mul_f32 v[180:181], v[180:181], s[26:27] op_sel_hi:[1,0]
	v_pk_mul_f32 v[182:183], v[182:183], s[26:27] op_sel_hi:[1,0]
	v_lshl_add_u64 v[178:179], v[178:179], 0, v[164:165]
	v_pk_mul_f32 v[190:191], v[190:191], s[26:27] op_sel_hi:[1,0]
	v_pk_mul_f32 v[192:193], v[192:193], s[26:27] op_sel_hi:[1,0]
	v_cvt_pk_bf16_f32 v180, v180, v181
	v_cvt_pk_bf16_f32 v181, v182, v183
	v_cvt_pk_bf16_f32 v182, v190, v191
	v_pk_mul_f32 v[190:191], v[74:75], s[24:25] op_sel_hi:[1,0]
	v_cvt_pk_bf16_f32 v183, v192, v193
	global_store_dwordx4 v[178:179], v[180:183], off
	v_pk_mul_f32 v[192:193], v[76:77], s[24:25] op_sel_hi:[1,0]
	v_exp_f32_e32 v190, v190
	v_pk_mul_f32 v[180:181], v[82:83], s[24:25] op_sel_hi:[1,0]
	v_pk_mul_f32 v[182:183], v[84:85], s[24:25] op_sel_hi:[1,0]
	v_exp_f32_e32 v180, v180
	v_exp_f32_e32 v181, v181
	v_exp_f32_e32 v182, v182
	v_exp_f32_e32 v183, v183
	v_exp_f32_e32 v191, v191
	v_exp_f32_e32 v192, v192
	v_exp_f32_e32 v193, v193
	v_pk_add_f32 v[180:181], v[180:181], 1.0 op_sel_hi:[1,0]
	v_pk_add_f32 v[182:183], v[182:183], 1.0 op_sel_hi:[1,0]
	v_rcp_f32_e32 v180, v180
	v_rcp_f32_e32 v181, v181
	v_rcp_f32_e32 v182, v182
	v_rcp_f32_e32 v183, v183
	v_pk_add_f32 v[190:191], v[190:191], 1.0 op_sel_hi:[1,0]
	v_pk_add_f32 v[192:193], v[192:193], 1.0 op_sel_hi:[1,0]
	v_rcp_f32_e32 v190, v190
	v_rcp_f32_e32 v191, v191
	v_rcp_f32_e32 v192, v192
	v_rcp_f32_e32 v193, v193
	v_pk_fma_f32 v[180:181], v[180:181], v[170:171], v[134:135]
	v_pk_fma_f32 v[182:183], v[182:183], v[172:173], v[136:137]
	v_max_f32_e32 v181, 0xda24260, v181
	v_max_f32_e32 v180, 0xda24260, v180
	v_max_f32_e32 v183, 0xda24260, v183
	v_max_f32_e32 v182, 0xda24260, v182
	v_pk_fma_f32 v[190:191], v[190:191], v[176:177], v[130:131]
	v_pk_fma_f32 v[192:193], v[192:193], v[174:175], v[132:133]
	v_log_f32_e32 v180, v180
	v_log_f32_e32 v181, v181
	v_log_f32_e32 v182, v182
	v_log_f32_e32 v183, v183
	v_max_f32_e32 v191, 0xda24260, v191
	v_max_f32_e32 v190, 0xda24260, v190
	v_max_f32_e32 v193, 0xda24260, v193
	v_max_f32_e32 v192, 0xda24260, v192
	v_log_f32_e32 v190, v190
	v_log_f32_e32 v191, v191
	v_log_f32_e32 v192, v192
	v_log_f32_e32 v193, v193
	v_pk_mul_f32 v[180:181], v[180:181], s[26:27] op_sel_hi:[1,0]
	v_pk_mul_f32 v[182:183], v[182:183], s[26:27] op_sel_hi:[1,0]
	v_pk_mul_f32 v[190:191], v[190:191], s[26:27] op_sel_hi:[1,0]
	v_pk_mul_f32 v[192:193], v[192:193], s[26:27] op_sel_hi:[1,0]
	v_cvt_pk_bf16_f32 v180, v180, v181
	v_cvt_pk_bf16_f32 v181, v182, v183
	v_cvt_pk_bf16_f32 v182, v190, v191
	v_pk_mul_f32 v[190:191], v[78:79], s[24:25] op_sel_hi:[1,0]
	v_cvt_pk_bf16_f32 v183, v192, v193
	global_store_dwordx4 v[178:179], v[180:183], off offset:256
	v_pk_mul_f32 v[192:193], v[80:81], s[24:25] op_sel_hi:[1,0]
	v_exp_f32_e32 v190, v190
	v_pk_mul_f32 v[180:181], v[86:87], s[24:25] op_sel_hi:[1,0]
	v_pk_mul_f32 v[182:183], v[88:89], s[24:25] op_sel_hi:[1,0]
	v_exp_f32_e32 v180, v180
	v_exp_f32_e32 v181, v181
	v_exp_f32_e32 v182, v182
	v_exp_f32_e32 v183, v183
	v_exp_f32_e32 v191, v191
	v_exp_f32_e32 v192, v192
	v_exp_f32_e32 v193, v193
	v_pk_add_f32 v[180:181], v[180:181], 1.0 op_sel_hi:[1,0]
	v_pk_add_f32 v[182:183], v[182:183], 1.0 op_sel_hi:[1,0]
	v_rcp_f32_e32 v180, v180
	v_rcp_f32_e32 v181, v181
	v_rcp_f32_e32 v182, v182
	v_rcp_f32_e32 v183, v183
	v_pk_add_f32 v[190:191], v[190:191], 1.0 op_sel_hi:[1,0]
	v_pk_add_f32 v[192:193], v[192:193], 1.0 op_sel_hi:[1,0]
	v_rcp_f32_e32 v190, v190
	v_rcp_f32_e32 v191, v191
	v_rcp_f32_e32 v192, v192
	v_rcp_f32_e32 v193, v193
	v_pk_fma_f32 v[180:181], v[180:181], v[158:159], v[142:143]
	v_pk_fma_f32 v[182:183], v[182:183], v[160:161], v[144:145]
	v_max_f32_e32 v181, 0xda24260, v181
	v_max_f32_e32 v180, 0xda24260, v180
	v_max_f32_e32 v183, 0xda24260, v183
	v_max_f32_e32 v182, 0xda24260, v182
	v_pk_fma_f32 v[190:191], v[190:191], v[166:167], v[138:139]
	v_pk_fma_f32 v[192:193], v[192:193], v[168:169], v[140:141]
	v_log_f32_e32 v180, v180
	v_log_f32_e32 v181, v181
	v_log_f32_e32 v182, v182
	v_log_f32_e32 v183, v183
	v_max_f32_e32 v191, 0xda24260, v191
	v_max_f32_e32 v190, 0xda24260, v190
	v_max_f32_e32 v193, 0xda24260, v193
	v_max_f32_e32 v192, 0xda24260, v192
	v_log_f32_e32 v190, v190
	v_log_f32_e32 v191, v191
	v_log_f32_e32 v192, v192
	v_log_f32_e32 v193, v193
	v_or_b32_e32 v178, 48, v189
	v_mad_i64_i32 v[178:179], s[2:3], v178, s17, v[162:163]
	v_pk_mul_f32 v[180:181], v[180:181], s[26:27] op_sel_hi:[1,0]
	v_pk_mul_f32 v[182:183], v[182:183], s[26:27] op_sel_hi:[1,0]
	v_lshl_add_u64 v[178:179], v[178:179], 0, v[164:165]
	v_pk_mul_f32 v[190:191], v[190:191], s[26:27] op_sel_hi:[1,0]
	v_pk_mul_f32 v[192:193], v[192:193], s[26:27] op_sel_hi:[1,0]
	v_cvt_pk_bf16_f32 v180, v180, v181
	v_cvt_pk_bf16_f32 v181, v182, v183
	v_cvt_pk_bf16_f32 v182, v190, v191
	v_pk_mul_f32 v[190:191], v[66:67], s[24:25] op_sel_hi:[1,0]
	v_cvt_pk_bf16_f32 v183, v192, v193
	global_store_dwordx4 v[178:179], v[180:183], off
	v_pk_mul_f32 v[192:193], v[68:69], s[24:25] op_sel_hi:[1,0]
	v_exp_f32_e32 v190, v190
	v_pk_mul_f32 v[180:181], v[70:71], s[24:25] op_sel_hi:[1,0]
	v_pk_mul_f32 v[182:183], v[72:73], s[24:25] op_sel_hi:[1,0]
	v_exp_f32_e32 v180, v180
	v_exp_f32_e32 v181, v181
	v_exp_f32_e32 v182, v182
	v_exp_f32_e32 v183, v183
	v_exp_f32_e32 v191, v191
	v_exp_f32_e32 v192, v192
	v_exp_f32_e32 v193, v193
	v_pk_add_f32 v[180:181], v[180:181], 1.0 op_sel_hi:[1,0]
	v_pk_add_f32 v[182:183], v[182:183], 1.0 op_sel_hi:[1,0]
	v_rcp_f32_e32 v180, v180
	v_rcp_f32_e32 v181, v181
	v_rcp_f32_e32 v182, v182
	v_rcp_f32_e32 v183, v183
	v_pk_add_f32 v[190:191], v[190:191], 1.0 op_sel_hi:[1,0]
	v_pk_add_f32 v[192:193], v[192:193], 1.0 op_sel_hi:[1,0]
	v_rcp_f32_e32 v190, v190
	v_rcp_f32_e32 v191, v191
	v_rcp_f32_e32 v192, v192
	v_rcp_f32_e32 v193, v193
	v_pk_fma_f32 v[180:181], v[180:181], v[170:171], v[134:135]
	v_pk_fma_f32 v[182:183], v[182:183], v[172:173], v[136:137]
	v_max_f32_e32 v181, 0xda24260, v181
	v_max_f32_e32 v180, 0xda24260, v180
	v_max_f32_e32 v183, 0xda24260, v183
	v_max_f32_e32 v182, 0xda24260, v182
	v_pk_fma_f32 v[190:191], v[190:191], v[176:177], v[130:131]
	v_pk_fma_f32 v[192:193], v[192:193], v[174:175], v[132:133]
	v_log_f32_e32 v180, v180
	v_log_f32_e32 v181, v181
	v_log_f32_e32 v182, v182
	v_log_f32_e32 v183, v183
	v_max_f32_e32 v191, 0xda24260, v191
	v_max_f32_e32 v190, 0xda24260, v190
	v_max_f32_e32 v193, 0xda24260, v193
	v_max_f32_e32 v192, 0xda24260, v192
	v_log_f32_e32 v190, v190
	v_log_f32_e32 v191, v191
	v_log_f32_e32 v192, v192
	v_log_f32_e32 v193, v193
	v_pk_mul_f32 v[180:181], v[180:181], s[26:27] op_sel_hi:[1,0]
	v_pk_mul_f32 v[182:183], v[182:183], s[26:27] op_sel_hi:[1,0]
	v_pk_mul_f32 v[190:191], v[190:191], s[26:27] op_sel_hi:[1,0]
	v_pk_mul_f32 v[192:193], v[192:193], s[26:27] op_sel_hi:[1,0]
	v_cvt_pk_bf16_f32 v180, v180, v181
	v_cvt_pk_bf16_f32 v181, v182, v183
	v_cvt_pk_bf16_f32 v182, v190, v191
	v_pk_mul_f32 v[190:191], v[56:57], s[24:25] op_sel_hi:[1,0]
	v_cvt_pk_bf16_f32 v183, v192, v193
	global_store_dwordx4 v[178:179], v[180:183], off offset:256
	v_pk_mul_f32 v[192:193], v[58:59], s[24:25] op_sel_hi:[1,0]
	v_exp_f32_e32 v190, v190
	v_pk_mul_f32 v[180:181], v[60:61], s[24:25] op_sel_hi:[1,0]
	v_pk_mul_f32 v[182:183], v[62:63], s[24:25] op_sel_hi:[1,0]
	v_exp_f32_e32 v180, v180
	v_exp_f32_e32 v181, v181
	v_exp_f32_e32 v182, v182
	v_exp_f32_e32 v183, v183
	v_exp_f32_e32 v191, v191
	v_exp_f32_e32 v192, v192
	v_exp_f32_e32 v193, v193
	v_pk_add_f32 v[180:181], v[180:181], 1.0 op_sel_hi:[1,0]
	v_pk_add_f32 v[182:183], v[182:183], 1.0 op_sel_hi:[1,0]
	v_rcp_f32_e32 v180, v180
	v_rcp_f32_e32 v181, v181
	v_rcp_f32_e32 v182, v182
	v_rcp_f32_e32 v183, v183
	v_pk_add_f32 v[190:191], v[190:191], 1.0 op_sel_hi:[1,0]
	v_pk_add_f32 v[192:193], v[192:193], 1.0 op_sel_hi:[1,0]
	v_rcp_f32_e32 v190, v190
	v_rcp_f32_e32 v191, v191
	v_rcp_f32_e32 v192, v192
	v_rcp_f32_e32 v193, v193
	v_pk_fma_f32 v[180:181], v[180:181], v[158:159], v[142:143]
	v_pk_fma_f32 v[182:183], v[182:183], v[160:161], v[144:145]
	v_max_f32_e32 v181, 0xda24260, v181
	v_max_f32_e32 v180, 0xda24260, v180
	v_max_f32_e32 v183, 0xda24260, v183
	v_max_f32_e32 v182, 0xda24260, v182
	v_pk_fma_f32 v[190:191], v[190:191], v[166:167], v[138:139]
	v_pk_fma_f32 v[192:193], v[192:193], v[168:169], v[140:141]
	v_log_f32_e32 v180, v180
	v_log_f32_e32 v181, v181
	v_log_f32_e32 v182, v182
	v_log_f32_e32 v183, v183
	v_max_f32_e32 v191, 0xda24260, v191
	v_max_f32_e32 v190, 0xda24260, v190
	v_max_f32_e32 v193, 0xda24260, v193
	v_max_f32_e32 v192, 0xda24260, v192
	v_log_f32_e32 v190, v190
	v_log_f32_e32 v191, v191
	v_log_f32_e32 v192, v192
	v_log_f32_e32 v193, v193
	v_add_u32_e32 v178, 0x80, v189
	v_mad_i64_i32 v[178:179], s[2:3], v178, s17, v[162:163]
	v_pk_mul_f32 v[180:181], v[180:181], s[26:27] op_sel_hi:[1,0]
	v_pk_mul_f32 v[182:183], v[182:183], s[26:27] op_sel_hi:[1,0]
	v_lshl_add_u64 v[178:179], v[178:179], 0, v[164:165]
	v_pk_mul_f32 v[190:191], v[190:191], s[26:27] op_sel_hi:[1,0]
	v_pk_mul_f32 v[192:193], v[192:193], s[26:27] op_sel_hi:[1,0]
	v_cvt_pk_bf16_f32 v180, v180, v181
	v_cvt_pk_bf16_f32 v181, v182, v183
	v_cvt_pk_bf16_f32 v182, v190, v191
	v_pk_mul_f32 v[190:191], v[40:41], s[24:25] op_sel_hi:[1,0]
	v_cvt_pk_bf16_f32 v183, v192, v193
	global_store_dwordx4 v[178:179], v[180:183], off
	v_pk_mul_f32 v[192:193], v[42:43], s[24:25] op_sel_hi:[1,0]
	v_exp_f32_e32 v190, v190
	v_pk_mul_f32 v[180:181], v[48:49], s[24:25] op_sel_hi:[1,0]
	v_pk_mul_f32 v[182:183], v[50:51], s[24:25] op_sel_hi:[1,0]
	v_exp_f32_e32 v180, v180
	v_exp_f32_e32 v181, v181
	v_exp_f32_e32 v182, v182
	v_exp_f32_e32 v183, v183
	v_exp_f32_e32 v191, v191
	v_exp_f32_e32 v192, v192
	v_exp_f32_e32 v193, v193
	v_pk_add_f32 v[180:181], v[180:181], 1.0 op_sel_hi:[1,0]
	v_pk_add_f32 v[182:183], v[182:183], 1.0 op_sel_hi:[1,0]
	v_rcp_f32_e32 v180, v180
	v_rcp_f32_e32 v181, v181
	v_rcp_f32_e32 v182, v182
	v_rcp_f32_e32 v183, v183
	v_pk_add_f32 v[190:191], v[190:191], 1.0 op_sel_hi:[1,0]
	v_pk_add_f32 v[192:193], v[192:193], 1.0 op_sel_hi:[1,0]
	v_rcp_f32_e32 v190, v190
	v_rcp_f32_e32 v191, v191
	v_rcp_f32_e32 v192, v192
	v_rcp_f32_e32 v193, v193
	v_pk_fma_f32 v[180:181], v[180:181], v[170:171], v[134:135]
	v_pk_fma_f32 v[182:183], v[182:183], v[172:173], v[136:137]
	v_max_f32_e32 v181, 0xda24260, v181
	v_max_f32_e32 v180, 0xda24260, v180
	v_max_f32_e32 v183, 0xda24260, v183
	v_max_f32_e32 v182, 0xda24260, v182
	v_pk_fma_f32 v[190:191], v[190:191], v[176:177], v[130:131]
	v_pk_fma_f32 v[192:193], v[192:193], v[174:175], v[132:133]
	v_log_f32_e32 v180, v180
	v_log_f32_e32 v181, v181
	v_log_f32_e32 v182, v182
	v_log_f32_e32 v183, v183
	v_max_f32_e32 v191, 0xda24260, v191
	v_max_f32_e32 v190, 0xda24260, v190
	v_max_f32_e32 v193, 0xda24260, v193
	v_max_f32_e32 v192, 0xda24260, v192
	v_log_f32_e32 v190, v190
	v_log_f32_e32 v191, v191
	v_log_f32_e32 v192, v192
	v_log_f32_e32 v193, v193
	v_pk_mul_f32 v[180:181], v[180:181], s[26:27] op_sel_hi:[1,0]
	v_pk_mul_f32 v[182:183], v[182:183], s[26:27] op_sel_hi:[1,0]
	v_pk_mul_f32 v[190:191], v[190:191], s[26:27] op_sel_hi:[1,0]
	v_pk_mul_f32 v[192:193], v[192:193], s[26:27] op_sel_hi:[1,0]
	v_cvt_pk_bf16_f32 v180, v180, v181
	v_cvt_pk_bf16_f32 v181, v182, v183
	v_cvt_pk_bf16_f32 v182, v190, v191
	v_pk_mul_f32 v[190:191], v[44:45], s[24:25] op_sel_hi:[1,0]
	v_cvt_pk_bf16_f32 v183, v192, v193
	global_store_dwordx4 v[178:179], v[180:183], off offset:256
	v_pk_mul_f32 v[192:193], v[46:47], s[24:25] op_sel_hi:[1,0]
	v_exp_f32_e32 v190, v190
	v_pk_mul_f32 v[180:181], v[52:53], s[24:25] op_sel_hi:[1,0]
	v_pk_mul_f32 v[182:183], v[54:55], s[24:25] op_sel_hi:[1,0]
	v_exp_f32_e32 v180, v180
	v_exp_f32_e32 v181, v181
	v_exp_f32_e32 v182, v182
	v_exp_f32_e32 v183, v183
	v_exp_f32_e32 v191, v191
	v_exp_f32_e32 v192, v192
	v_exp_f32_e32 v193, v193
	v_pk_add_f32 v[180:181], v[180:181], 1.0 op_sel_hi:[1,0]
	v_pk_add_f32 v[182:183], v[182:183], 1.0 op_sel_hi:[1,0]
	v_rcp_f32_e32 v180, v180
	v_rcp_f32_e32 v181, v181
	v_rcp_f32_e32 v182, v182
	v_rcp_f32_e32 v183, v183
	v_pk_add_f32 v[190:191], v[190:191], 1.0 op_sel_hi:[1,0]
	v_pk_add_f32 v[192:193], v[192:193], 1.0 op_sel_hi:[1,0]
	v_rcp_f32_e32 v190, v190
	v_rcp_f32_e32 v191, v191
	v_rcp_f32_e32 v192, v192
	v_rcp_f32_e32 v193, v193
	v_pk_fma_f32 v[180:181], v[180:181], v[158:159], v[142:143]
	v_pk_fma_f32 v[182:183], v[182:183], v[160:161], v[144:145]
	v_max_f32_e32 v181, 0xda24260, v181
	v_max_f32_e32 v180, 0xda24260, v180
	v_max_f32_e32 v183, 0xda24260, v183
	v_max_f32_e32 v182, 0xda24260, v182
	v_pk_fma_f32 v[190:191], v[190:191], v[166:167], v[138:139]
	v_pk_fma_f32 v[192:193], v[192:193], v[168:169], v[140:141]
	v_log_f32_e32 v180, v180
	v_log_f32_e32 v181, v181
	v_log_f32_e32 v182, v182
	v_log_f32_e32 v183, v183
	v_max_f32_e32 v191, 0xda24260, v191
	v_max_f32_e32 v190, 0xda24260, v190
	v_max_f32_e32 v193, 0xda24260, v193
	v_max_f32_e32 v192, 0xda24260, v192
	v_log_f32_e32 v190, v190
	v_log_f32_e32 v191, v191
	v_log_f32_e32 v192, v192
	v_log_f32_e32 v193, v193
	v_add_u32_e32 v178, 0x90, v189
	v_mad_i64_i32 v[178:179], s[2:3], v178, s17, v[162:163]
	v_pk_mul_f32 v[180:181], v[180:181], s[26:27] op_sel_hi:[1,0]
	v_pk_mul_f32 v[182:183], v[182:183], s[26:27] op_sel_hi:[1,0]
	v_lshl_add_u64 v[178:179], v[178:179], 0, v[164:165]
	v_pk_mul_f32 v[190:191], v[190:191], s[26:27] op_sel_hi:[1,0]
	v_pk_mul_f32 v[192:193], v[192:193], s[26:27] op_sel_hi:[1,0]
	v_cvt_pk_bf16_f32 v180, v180, v181
	v_cvt_pk_bf16_f32 v181, v182, v183
	v_cvt_pk_bf16_f32 v182, v190, v191
	v_pk_mul_f32 v[190:191], v[24:25], s[24:25] op_sel_hi:[1,0]
	v_cvt_pk_bf16_f32 v183, v192, v193
	global_store_dwordx4 v[178:179], v[180:183], off
	v_pk_mul_f32 v[192:193], v[26:27], s[24:25] op_sel_hi:[1,0]
	v_exp_f32_e32 v190, v190
	v_pk_mul_f32 v[180:181], v[32:33], s[24:25] op_sel_hi:[1,0]
	v_pk_mul_f32 v[182:183], v[34:35], s[24:25] op_sel_hi:[1,0]
	v_exp_f32_e32 v180, v180
	v_exp_f32_e32 v181, v181
	v_exp_f32_e32 v182, v182
	v_exp_f32_e32 v183, v183
	v_exp_f32_e32 v191, v191
	v_exp_f32_e32 v192, v192
	v_exp_f32_e32 v193, v193
	v_pk_add_f32 v[180:181], v[180:181], 1.0 op_sel_hi:[1,0]
	v_pk_add_f32 v[182:183], v[182:183], 1.0 op_sel_hi:[1,0]
	v_rcp_f32_e32 v180, v180
	v_rcp_f32_e32 v181, v181
	v_rcp_f32_e32 v182, v182
	v_rcp_f32_e32 v183, v183
	v_pk_add_f32 v[190:191], v[190:191], 1.0 op_sel_hi:[1,0]
	v_pk_add_f32 v[192:193], v[192:193], 1.0 op_sel_hi:[1,0]
	v_rcp_f32_e32 v190, v190
	v_rcp_f32_e32 v191, v191
	v_rcp_f32_e32 v192, v192
	v_rcp_f32_e32 v193, v193
	v_pk_fma_f32 v[180:181], v[180:181], v[170:171], v[134:135]
	v_pk_fma_f32 v[182:183], v[182:183], v[172:173], v[136:137]
	v_max_f32_e32 v181, 0xda24260, v181
	v_max_f32_e32 v180, 0xda24260, v180
	v_max_f32_e32 v183, 0xda24260, v183
	v_max_f32_e32 v182, 0xda24260, v182
	v_pk_fma_f32 v[190:191], v[190:191], v[176:177], v[130:131]
	v_pk_fma_f32 v[192:193], v[192:193], v[174:175], v[132:133]
	v_log_f32_e32 v180, v180
	v_log_f32_e32 v181, v181
	v_log_f32_e32 v182, v182
	v_log_f32_e32 v183, v183
	v_max_f32_e32 v191, 0xda24260, v191
	v_max_f32_e32 v190, 0xda24260, v190
	v_max_f32_e32 v193, 0xda24260, v193
	v_max_f32_e32 v192, 0xda24260, v192
	v_log_f32_e32 v190, v190
	v_log_f32_e32 v191, v191
	v_log_f32_e32 v192, v192
	v_log_f32_e32 v193, v193
	v_pk_mul_f32 v[180:181], v[180:181], s[26:27] op_sel_hi:[1,0]
	v_pk_mul_f32 v[182:183], v[182:183], s[26:27] op_sel_hi:[1,0]
	v_pk_mul_f32 v[190:191], v[190:191], s[26:27] op_sel_hi:[1,0]
	v_pk_mul_f32 v[192:193], v[192:193], s[26:27] op_sel_hi:[1,0]
	v_cvt_pk_bf16_f32 v180, v180, v181
	v_cvt_pk_bf16_f32 v181, v182, v183
	v_cvt_pk_bf16_f32 v182, v190, v191
	v_pk_mul_f32 v[190:191], v[28:29], s[24:25] op_sel_hi:[1,0]
	v_cvt_pk_bf16_f32 v183, v192, v193
	global_store_dwordx4 v[178:179], v[180:183], off offset:256
	v_pk_mul_f32 v[192:193], v[30:31], s[24:25] op_sel_hi:[1,0]
	v_exp_f32_e32 v190, v190
	v_pk_mul_f32 v[180:181], v[36:37], s[24:25] op_sel_hi:[1,0]
	v_pk_mul_f32 v[182:183], v[38:39], s[24:25] op_sel_hi:[1,0]
	v_exp_f32_e32 v180, v180
	v_exp_f32_e32 v181, v181
	v_exp_f32_e32 v182, v182
	v_exp_f32_e32 v183, v183
	v_exp_f32_e32 v191, v191
	v_exp_f32_e32 v192, v192
	v_exp_f32_e32 v193, v193
	v_pk_add_f32 v[180:181], v[180:181], 1.0 op_sel_hi:[1,0]
	v_pk_add_f32 v[182:183], v[182:183], 1.0 op_sel_hi:[1,0]
	v_rcp_f32_e32 v180, v180
	v_rcp_f32_e32 v181, v181
	v_rcp_f32_e32 v182, v182
	v_rcp_f32_e32 v183, v183
	v_pk_add_f32 v[190:191], v[190:191], 1.0 op_sel_hi:[1,0]
	v_pk_add_f32 v[192:193], v[192:193], 1.0 op_sel_hi:[1,0]
	v_rcp_f32_e32 v190, v190
	v_rcp_f32_e32 v191, v191
	v_rcp_f32_e32 v192, v192
	v_rcp_f32_e32 v193, v193
	v_pk_fma_f32 v[180:181], v[180:181], v[158:159], v[142:143]
	v_pk_fma_f32 v[182:183], v[182:183], v[160:161], v[144:145]
	v_max_f32_e32 v181, 0xda24260, v181
	v_max_f32_e32 v180, 0xda24260, v180
	v_max_f32_e32 v183, 0xda24260, v183
	v_max_f32_e32 v182, 0xda24260, v182
	v_pk_fma_f32 v[190:191], v[190:191], v[166:167], v[138:139]
	v_pk_fma_f32 v[192:193], v[192:193], v[168:169], v[140:141]
	v_log_f32_e32 v180, v180
	v_log_f32_e32 v181, v181
	v_log_f32_e32 v182, v182
	v_log_f32_e32 v183, v183
	v_max_f32_e32 v191, 0xda24260, v191
	v_max_f32_e32 v190, 0xda24260, v190
	v_max_f32_e32 v193, 0xda24260, v193
	v_max_f32_e32 v192, 0xda24260, v192
	v_log_f32_e32 v190, v190
	v_log_f32_e32 v191, v191
	v_log_f32_e32 v192, v192
	v_log_f32_e32 v193, v193
	v_add_u32_e32 v178, 0xa0, v189
	v_mad_i64_i32 v[178:179], s[2:3], v178, s17, v[162:163]
	v_pk_mul_f32 v[180:181], v[180:181], s[26:27] op_sel_hi:[1,0]
	v_pk_mul_f32 v[182:183], v[182:183], s[26:27] op_sel_hi:[1,0]
	v_lshl_add_u64 v[178:179], v[178:179], 0, v[164:165]
	v_pk_mul_f32 v[190:191], v[190:191], s[26:27] op_sel_hi:[1,0]
	v_pk_mul_f32 v[192:193], v[192:193], s[26:27] op_sel_hi:[1,0]
	v_cvt_pk_bf16_f32 v180, v180, v181
	v_cvt_pk_bf16_f32 v181, v182, v183
	v_cvt_pk_bf16_f32 v182, v190, v191
	v_pk_mul_f32 v[190:191], v[8:9], s[24:25] op_sel_hi:[1,0]
	v_cvt_pk_bf16_f32 v183, v192, v193
	global_store_dwordx4 v[178:179], v[180:183], off
	v_pk_mul_f32 v[192:193], v[10:11], s[24:25] op_sel_hi:[1,0]
	v_exp_f32_e32 v190, v190
	v_pk_mul_f32 v[180:181], v[16:17], s[24:25] op_sel_hi:[1,0]
	v_pk_mul_f32 v[182:183], v[18:19], s[24:25] op_sel_hi:[1,0]
	v_exp_f32_e32 v180, v180
	v_exp_f32_e32 v181, v181
	v_exp_f32_e32 v182, v182
	v_exp_f32_e32 v183, v183
	v_exp_f32_e32 v191, v191
	v_exp_f32_e32 v192, v192
	v_exp_f32_e32 v193, v193
	v_pk_add_f32 v[180:181], v[180:181], 1.0 op_sel_hi:[1,0]
	v_pk_add_f32 v[182:183], v[182:183], 1.0 op_sel_hi:[1,0]
	v_rcp_f32_e32 v180, v180
	v_rcp_f32_e32 v181, v181
	v_rcp_f32_e32 v182, v182
	v_rcp_f32_e32 v183, v183
	v_pk_add_f32 v[190:191], v[190:191], 1.0 op_sel_hi:[1,0]
	v_pk_add_f32 v[192:193], v[192:193], 1.0 op_sel_hi:[1,0]
	v_rcp_f32_e32 v190, v190
	v_rcp_f32_e32 v191, v191
	v_rcp_f32_e32 v192, v192
	v_rcp_f32_e32 v193, v193
	v_pk_fma_f32 v[180:181], v[180:181], v[170:171], v[134:135]
	v_pk_fma_f32 v[182:183], v[182:183], v[172:173], v[136:137]
	v_max_f32_e32 v181, 0xda24260, v181
	v_max_f32_e32 v180, 0xda24260, v180
	v_max_f32_e32 v183, 0xda24260, v183
	v_max_f32_e32 v182, 0xda24260, v182
	v_pk_fma_f32 v[190:191], v[190:191], v[176:177], v[130:131]
	v_pk_fma_f32 v[192:193], v[192:193], v[174:175], v[132:133]
	v_log_f32_e32 v180, v180
	v_log_f32_e32 v181, v181
	v_log_f32_e32 v182, v182
	v_log_f32_e32 v183, v183
	v_max_f32_e32 v191, 0xda24260, v191
	v_max_f32_e32 v190, 0xda24260, v190
	v_max_f32_e32 v193, 0xda24260, v193
	v_max_f32_e32 v192, 0xda24260, v192
	v_log_f32_e32 v190, v190
	v_log_f32_e32 v191, v191
	v_log_f32_e32 v192, v192
	v_log_f32_e32 v193, v193
	v_pk_mul_f32 v[180:181], v[180:181], s[26:27] op_sel_hi:[1,0]
	v_pk_mul_f32 v[182:183], v[182:183], s[26:27] op_sel_hi:[1,0]
	v_pk_mul_f32 v[190:191], v[190:191], s[26:27] op_sel_hi:[1,0]
	v_pk_mul_f32 v[192:193], v[192:193], s[26:27] op_sel_hi:[1,0]
	v_cvt_pk_bf16_f32 v180, v180, v181
	v_cvt_pk_bf16_f32 v181, v182, v183
	v_cvt_pk_bf16_f32 v182, v190, v191
	s_nop 0
	v_cvt_pk_bf16_f32 v183, v192, v193
	global_store_dwordx4 v[178:179], v[180:183], off offset:256
	v_add_u32_e32 v178, 0xb0, v189
	v_mad_i64_i32 v[162:163], s[2:3], v178, s17, v[162:163]
	v_lshl_add_u64 v[162:163], v[162:163], 0, v[164:165]
	v_pk_mul_f32 v[164:165], v[20:21], s[24:25] op_sel_hi:[1,0]
	s_nop 0
	v_exp_f32_e32 v164, v164
	v_exp_f32_e32 v165, v165
	s_nop 0
	v_pk_add_f32 v[164:165], v[164:165], 1.0 op_sel_hi:[1,0]
	s_nop 0
	v_rcp_f32_e32 v164, v164
	v_rcp_f32_e32 v165, v165
	s_nop 0
	v_pk_fma_f32 v[142:143], v[164:165], v[158:159], v[142:143]
	v_pk_mul_f32 v[158:159], v[22:23], s[24:25] op_sel_hi:[1,0]
	v_max_f32_e32 v143, 0xda24260, v143
	v_exp_f32_e32 v158, v158
	v_exp_f32_e32 v159, v159
	v_max_f32_e32 v142, 0xda24260, v142
	v_log_f32_e32 v142, v142
	v_log_f32_e32 v143, v143
	v_pk_add_f32 v[158:159], v[158:159], 1.0 op_sel_hi:[1,0]
	v_pk_mul_f32 v[142:143], v[142:143], s[26:27] op_sel_hi:[1,0]
	v_rcp_f32_e32 v158, v158
	v_rcp_f32_e32 v159, v159
	s_nop 0
	v_pk_fma_f32 v[144:145], v[158:159], v[160:161], v[144:145]
	v_pk_mul_f32 v[158:159], v[12:13], s[24:25] op_sel_hi:[1,0]
	v_max_f32_e32 v145, 0xda24260, v145
	v_exp_f32_e32 v158, v158
	v_exp_f32_e32 v159, v159
	v_max_f32_e32 v144, 0xda24260, v144
	v_log_f32_e32 v144, v144
	v_log_f32_e32 v145, v145
	v_pk_add_f32 v[158:159], v[158:159], 1.0 op_sel_hi:[1,0]
	v_pk_mul_f32 v[144:145], v[144:145], s[26:27] op_sel_hi:[1,0]
	v_rcp_f32_e32 v158, v158
	v_rcp_f32_e32 v159, v159
	s_nop 0
	v_pk_fma_f32 v[138:139], v[158:159], v[166:167], v[138:139]
	s_nop 0
	v_max_f32_e32 v139, 0xda24260, v139
	v_max_f32_e32 v138, 0xda24260, v138
	v_log_f32_e32 v138, v138
	v_log_f32_e32 v139, v139
	s_nop 0
	v_pk_mul_f32 v[158:159], v[138:139], s[26:27] op_sel_hi:[1,0]
	v_pk_mul_f32 v[138:139], v[14:15], s[24:25] op_sel_hi:[1,0]
	s_nop 0
	v_exp_f32_e32 v138, v138
	v_exp_f32_e32 v139, v139
	s_nop 0
	v_pk_add_f32 v[138:139], v[138:139], 1.0 op_sel_hi:[1,0]
	s_nop 0
	v_rcp_f32_e32 v138, v138
	v_rcp_f32_e32 v139, v139
	s_nop 0
	v_pk_fma_f32 v[138:139], v[138:139], v[168:169], v[140:141]
	s_nop 0
	v_max_f32_e32 v139, 0xda24260, v139
	v_max_f32_e32 v138, 0xda24260, v138
	v_log_f32_e32 v138, v138
	v_log_f32_e32 v139, v139
	s_nop 0
	v_pk_mul_f32 v[160:161], v[138:139], s[26:27] op_sel_hi:[1,0]
	v_cvt_pk_bf16_f32 v138, v142, v143
	v_cvt_pk_bf16_f32 v139, v144, v145
	v_cvt_pk_bf16_f32 v140, v158, v159
	s_nop 0
	v_cvt_pk_bf16_f32 v141, v160, v161
	global_store_dwordx4 v[162:163], v[138:141], off
	s_nop 1
	v_pk_mul_f32 v[138:139], v[4:5], s[24:25] op_sel_hi:[1,0]
	s_nop 0
	v_exp_f32_e32 v138, v138
	v_exp_f32_e32 v139, v139
	s_nop 0
	v_pk_add_f32 v[138:139], v[138:139], 1.0 op_sel_hi:[1,0]
	s_nop 0
	v_rcp_f32_e32 v138, v138
	v_rcp_f32_e32 v139, v139
	s_nop 0
	v_pk_fma_f32 v[134:135], v[138:139], v[170:171], v[134:135]
	v_pk_mul_f32 v[138:139], v[6:7], s[24:25] op_sel_hi:[1,0]
	v_max_f32_e32 v135, 0xda24260, v135
	v_exp_f32_e32 v138, v138
	v_exp_f32_e32 v139, v139
	v_max_f32_e32 v134, 0xda24260, v134
	v_log_f32_e32 v134, v134
	v_log_f32_e32 v135, v135
	v_pk_add_f32 v[138:139], v[138:139], 1.0 op_sel_hi:[1,0]
	v_pk_mul_f32 v[134:135], v[134:135], s[26:27] op_sel_hi:[1,0]
	v_rcp_f32_e32 v138, v138
	v_rcp_f32_e32 v139, v139
	s_nop 0
	v_pk_fma_f32 v[136:137], v[138:139], v[172:173], v[136:137]
	v_pk_mul_f32 v[138:139], v[0:1], s[24:25] op_sel_hi:[1,0]
	v_max_f32_e32 v137, 0xda24260, v137
	v_exp_f32_e32 v138, v138
	v_exp_f32_e32 v139, v139
	v_max_f32_e32 v136, 0xda24260, v136
	v_log_f32_e32 v136, v136
	v_log_f32_e32 v137, v137
	v_pk_add_f32 v[138:139], v[138:139], 1.0 op_sel_hi:[1,0]
	v_pk_mul_f32 v[136:137], v[136:137], s[26:27] op_sel_hi:[1,0]
	v_rcp_f32_e32 v138, v138
	v_rcp_f32_e32 v139, v139
	s_nop 0
	v_pk_fma_f32 v[130:131], v[138:139], v[176:177], v[130:131]
	s_nop 0
	v_max_f32_e32 v131, 0xda24260, v131
	v_max_f32_e32 v130, 0xda24260, v130
	v_log_f32_e32 v130, v130
	v_log_f32_e32 v131, v131
	s_nop 0
	v_pk_mul_f32 v[138:139], v[130:131], s[26:27] op_sel_hi:[1,0]
	v_pk_mul_f32 v[130:131], v[2:3], s[24:25] op_sel_hi:[1,0]
	s_nop 0
	v_exp_f32_e32 v130, v130
	v_exp_f32_e32 v131, v131
	s_nop 0
	v_pk_add_f32 v[130:131], v[130:131], 1.0 op_sel_hi:[1,0]
	s_nop 0
	v_rcp_f32_e32 v130, v130
	v_rcp_f32_e32 v131, v131
	s_nop 0
	v_pk_fma_f32 v[130:131], v[130:131], v[174:175], v[132:133]
	s_nop 0
	v_max_f32_e32 v131, 0xda24260, v131
	v_max_f32_e32 v130, 0xda24260, v130
	v_log_f32_e32 v130, v130
	v_log_f32_e32 v131, v131
	s_nop 0
	v_pk_mul_f32 v[140:141], v[130:131], s[26:27] op_sel_hi:[1,0]
	v_cvt_pk_bf16_f32 v130, v134, v135
	v_cvt_pk_bf16_f32 v131, v136, v137
	v_cvt_pk_bf16_f32 v132, v138, v139
	s_nop 0
	v_cvt_pk_bf16_f32 v133, v140, v141

.Lg1ls_fast:
	s_lshl_b32 s2, s2, 9
	v_subrev_u32_e32 v130, s2, v64
	v_ashrrev_i32_e32 v131, 31, v130
	v_lshl_add_u64 v[134:135], v[130:131], 2, s[10:11]
	global_load_dwordx4 v[138:141], v[134:135], off offset:16
	global_load_dwordx4 v[142:145], v[134:135], off
	global_load_dwordx4 v[130:133], v[134:135], off offset:528
	s_nop 0
	global_load_dwordx4 v[134:137], v[134:135], off offset:512
	v_ashrrev_i32_e32 v169, 31, v64
	v_mov_b32_e32 v168, v64
	s_mov_b32 s24, 0xbfb8aa3b
	v_lshlrev_b64 v[168:169], 1, v[168:169]
	v_mov_b64_e32 v[166:167], s[8:9]
	s_movk_i32 s17, 0x2400
	s_mov_b32 s26, 0x3f317218
	s_waitcnt vmcnt(0)
	v_pk_add_f32 v[212:213], v[142:143], 1.0 op_sel_hi:[1,0] neg_lo:[1,0] neg_hi:[1,0]
	v_pk_add_f32 v[214:215], v[144:145], 1.0 op_sel_hi:[1,0] neg_lo:[1,0] neg_hi:[1,0]
	v_pk_add_f32 v[216:217], v[138:139], 1.0 op_sel_hi:[1,0] neg_lo:[1,0] neg_hi:[1,0]
	v_pk_add_f32 v[218:219], v[140:141], 1.0 op_sel_hi:[1,0] neg_lo:[1,0] neg_hi:[1,0]
	v_pk_add_f32 v[220:221], v[134:135], 1.0 op_sel_hi:[1,0] neg_lo:[1,0] neg_hi:[1,0]
	v_pk_add_f32 v[222:223], v[136:137], 1.0 op_sel_hi:[1,0] neg_lo:[1,0] neg_hi:[1,0]
	v_pk_add_f32 v[224:225], v[130:131], 1.0 op_sel_hi:[1,0] neg_lo:[1,0] neg_hi:[1,0]
	v_pk_add_f32 v[226:227], v[132:133], 1.0 op_sel_hi:[1,0] neg_lo:[1,0] neg_hi:[1,0]
	v_mov_b32_e32 v170, v189
	v_mad_i64_i32 v[170:171], s[2:3], v170, s17, v[166:167]
	v_lshl_add_u64 v[170:171], v[170:171], 0, v[168:169]
	v_pk_mul_f32 v[172:173], v[126:127], s[24:25] op_sel_hi:[1,0]
	v_pk_mul_f32 v[174:175], v[128:129], s[24:25] op_sel_hi:[1,0]
	v_pk_mul_f32 v[176:177], v[122:123], s[24:25] op_sel_hi:[1,0]
	v_pk_mul_f32 v[178:179], v[124:125], s[24:25] op_sel_hi:[1,0]
	v_exp_f32_e32 v172, v172
	v_exp_f32_e32 v173, v173
	v_exp_f32_e32 v174, v174
	v_exp_f32_e32 v175, v175
	v_exp_f32_e32 v176, v176
	v_exp_f32_e32 v177, v177
	v_exp_f32_e32 v178, v178
	v_exp_f32_e32 v179, v179
	v_pk_add_f32 v[172:173], v[172:173], 1.0 op_sel_hi:[1,0]
	v_pk_add_f32 v[174:175], v[174:175], 1.0 op_sel_hi:[1,0]
	v_pk_add_f32 v[176:177], v[176:177], 1.0 op_sel_hi:[1,0]
	v_pk_add_f32 v[178:179], v[178:179], 1.0 op_sel_hi:[1,0]
	v_rcp_f32_e32 v172, v172
	v_rcp_f32_e32 v173, v173
	v_rcp_f32_e32 v174, v174
	v_rcp_f32_e32 v175, v175
	v_rcp_f32_e32 v176, v176
	v_rcp_f32_e32 v177, v177
	v_rcp_f32_e32 v178, v178
	v_rcp_f32_e32 v179, v179
	v_pk_fma_f32 v[172:173], v[172:173], v[212:213], v[142:143]
	v_pk_fma_f32 v[174:175], v[174:175], v[214:215], v[144:145]
	v_pk_fma_f32 v[176:177], v[176:177], v[216:217], v[138:139]
	v_pk_fma_f32 v[178:179], v[178:179], v[218:219], v[140:141]
	v_max_f32_e32 v173, 0xda24260, v173
	v_max_f32_e32 v172, 0xda24260, v172
	v_max_f32_e32 v175, 0xda24260, v175
	v_max_f32_e32 v174, 0xda24260, v174
	v_max_f32_e32 v177, 0xda24260, v177
	v_max_f32_e32 v176, 0xda24260, v176
	v_max_f32_e32 v179, 0xda24260, v179
	v_max_f32_e32 v178, 0xda24260, v178
	v_log_f32_e32 v172, v172
	v_log_f32_e32 v173, v173
	v_log_f32_e32 v174, v174
	v_log_f32_e32 v175, v175
	v_log_f32_e32 v176, v176
	v_log_f32_e32 v177, v177
	v_log_f32_e32 v178, v178
	v_log_f32_e32 v179, v179
	v_pk_mul_f32 v[172:173], v[172:173], s[26:27] op_sel_hi:[1,0]
	v_pk_mul_f32 v[174:175], v[174:175], s[26:27] op_sel_hi:[1,0]
	v_pk_mul_f32 v[176:177], v[176:177], s[26:27] op_sel_hi:[1,0]
	v_pk_mul_f32 v[178:179], v[178:179], s[26:27] op_sel_hi:[1,0]
	v_cvt_pk_bf16_f32 v180, v172, v173
	v_cvt_pk_bf16_f32 v181, v174, v175
	v_cvt_pk_bf16_f32 v182, v176, v177
	v_cvt_pk_bf16_f32 v183, v178, v179
	global_store_dwordx4 v[170:171], v[180:183], off
	v_pk_mul_f32 v[172:173], v[114:115], s[24:25] op_sel_hi:[1,0]
	v_pk_mul_f32 v[174:175], v[116:117], s[24:25] op_sel_hi:[1,0]
	v_pk_mul_f32 v[176:177], v[106:107], s[24:25] op_sel_hi:[1,0]
	v_pk_mul_f32 v[178:179], v[108:109], s[24:25] op_sel_hi:[1,0]
	v_exp_f32_e32 v172, v172
	v_exp_f32_e32 v173, v173
	v_exp_f32_e32 v174, v174
	v_exp_f32_e32 v175, v175
	v_exp_f32_e32 v176, v176
	v_exp_f32_e32 v177, v177
	v_exp_f32_e32 v178, v178
	v_exp_f32_e32 v179, v179
	v_pk_add_f32 v[172:173], v[172:173], 1.0 op_sel_hi:[1,0]
	v_pk_add_f32 v[174:175], v[174:175], 1.0 op_sel_hi:[1,0]
	v_pk_add_f32 v[176:177], v[176:177], 1.0 op_sel_hi:[1,0]
	v_pk_add_f32 v[178:179], v[178:179], 1.0 op_sel_hi:[1,0]
	v_rcp_f32_e32 v172, v172
	v_rcp_f32_e32 v173, v173
	v_rcp_f32_e32 v174, v174
	v_rcp_f32_e32 v175, v175
	v_rcp_f32_e32 v176, v176
	v_rcp_f32_e32 v177, v177
	v_rcp_f32_e32 v178, v178
	v_rcp_f32_e32 v179, v179
	v_pk_fma_f32 v[172:173], v[172:173], v[220:221], v[134:135]
	v_pk_fma_f32 v[174:175], v[174:175], v[222:223], v[136:137]
	v_pk_fma_f32 v[176:177], v[176:177], v[224:225], v[130:131]
	v_pk_fma_f32 v[178:179], v[178:179], v[226:227], v[132:133]
	v_max_f32_e32 v173, 0xda24260, v173
	v_max_f32_e32 v172, 0xda24260, v172
	v_max_f32_e32 v175, 0xda24260, v175
	v_max_f32_e32 v174, 0xda24260, v174
	v_max_f32_e32 v177, 0xda24260, v177
	v_max_f32_e32 v176, 0xda24260, v176
	v_max_f32_e32 v179, 0xda24260, v179
	v_max_f32_e32 v178, 0xda24260, v178
	v_log_f32_e32 v172, v172
	v_log_f32_e32 v173, v173
	v_log_f32_e32 v174, v174
	v_log_f32_e32 v175, v175
	v_log_f32_e32 v176, v176
	v_log_f32_e32 v177, v177
	v_log_f32_e32 v178, v178
	v_log_f32_e32 v179, v179
	v_pk_mul_f32 v[172:173], v[172:173], s[26:27] op_sel_hi:[1,0]
	v_pk_mul_f32 v[174:175], v[174:175], s[26:27] op_sel_hi:[1,0]
	v_pk_mul_f32 v[176:177], v[176:177], s[26:27] op_sel_hi:[1,0]
	v_pk_mul_f32 v[178:179], v[178:179], s[26:27] op_sel_hi:[1,0]
	v_cvt_pk_bf16_f32 v180, v172, v173
	v_cvt_pk_bf16_f32 v181, v174, v175
	v_cvt_pk_bf16_f32 v182, v176, v177
	v_cvt_pk_bf16_f32 v183, v178, v179
	global_store_dwordx4 v[170:171], v[180:183], off offset:256
	v_add_u32_e32 v170, 16, v189
	v_mad_i64_i32 v[170:171], s[2:3], v170, s17, v[166:167]
	v_lshl_add_u64 v[170:171], v[170:171], 0, v[168:169]
	v_pk_mul_f32 v[172:173], v[118:119], s[24:25] op_sel_hi:[1,0]
	v_pk_mul_f32 v[174:175], v[120:121], s[24:25] op_sel_hi:[1,0]
	v_pk_mul_f32 v[176:177], v[110:111], s[24:25] op_sel_hi:[1,0]
	v_pk_mul_f32 v[178:179], v[112:113], s[24:25] op_sel_hi:[1,0]
	v_exp_f32_e32 v172, v172
	v_exp_f32_e32 v173, v173
	v_exp_f32_e32 v174, v174
	v_exp_f32_e32 v175, v175
	v_exp_f32_e32 v176, v176
	v_exp_f32_e32 v177, v177
	v_exp_f32_e32 v178, v178
	v_exp_f32_e32 v179, v179
	v_pk_add_f32 v[172:173], v[172:173], 1.0 op_sel_hi:[1,0]
	v_pk_add_f32 v[174:175], v[174:175], 1.0 op_sel_hi:[1,0]
	v_pk_add_f32 v[176:177], v[176:177], 1.0 op_sel_hi:[1,0]
	v_pk_add_f32 v[178:179], v[178:179], 1.0 op_sel_hi:[1,0]
	v_rcp_f32_e32 v172, v172
	v_rcp_f32_e32 v173, v173
	v_rcp_f32_e32 v174, v174
	v_rcp_f32_e32 v175, v175
	v_rcp_f32_e32 v176, v176
	v_rcp_f32_e32 v177, v177
	v_rcp_f32_e32 v178, v178
	v_rcp_f32_e32 v179, v179
	v_pk_fma_f32 v[172:173], v[172:173], v[212:213], v[142:143]
	v_pk_fma_f32 v[174:175], v[174:175], v[214:215], v[144:145]
	v_pk_fma_f32 v[176:177], v[176:177], v[216:217], v[138:139]
	v_pk_fma_f32 v[178:179], v[178:179], v[218:219], v[140:141]
	v_max_f32_e32 v173, 0xda24260, v173
	v_max_f32_e32 v172, 0xda24260, v172
	v_max_f32_e32 v175, 0xda24260, v175
	v_max_f32_e32 v174, 0xda24260, v174
	v_max_f32_e32 v177, 0xda24260, v177
	v_max_f32_e32 v176, 0xda24260, v176
	v_max_f32_e32 v179, 0xda24260, v179
	v_max_f32_e32 v178, 0xda24260, v178
	v_log_f32_e32 v172, v172
	v_log_f32_e32 v173, v173
	v_log_f32_e32 v174, v174
	v_log_f32_e32 v175, v175
	v_log_f32_e32 v176, v176
	v_log_f32_e32 v177, v177
	v_log_f32_e32 v178, v178
	v_log_f32_e32 v179, v179
	v_pk_mul_f32 v[172:173], v[172:173], s[26:27] op_sel_hi:[1,0]
	v_pk_mul_f32 v[174:175], v[174:175], s[26:27] op_sel_hi:[1,0]
	v_pk_mul_f32 v[176:177], v[176:177], s[26:27] op_sel_hi:[1,0]
	v_pk_mul_f32 v[178:179], v[178:179], s[26:27] op_sel_hi:[1,0]
	v_cvt_pk_bf16_f32 v180, v172, v173
	v_cvt_pk_bf16_f32 v181, v174, v175
	v_cvt_pk_bf16_f32 v182, v176, v177
	v_cvt_pk_bf16_f32 v183, v178, v179
	global_store_dwordx4 v[170:171], v[180:183], off
	v_pk_mul_f32 v[172:173], v[98:99], s[24:25] op_sel_hi:[1,0]
	v_pk_mul_f32 v[174:175], v[100:101], s[24:25] op_sel_hi:[1,0]
	v_pk_mul_f32 v[176:177], v[90:91], s[24:25] op_sel_hi:[1,0]
	v_pk_mul_f32 v[178:179], v[92:93], s[24:25] op_sel_hi:[1,0]
	v_exp_f32_e32 v172, v172
	v_exp_f32_e32 v173, v173
	v_exp_f32_e32 v174, v174
	v_exp_f32_e32 v175, v175
	v_exp_f32_e32 v176, v176
	v_exp_f32_e32 v177, v177
	v_exp_f32_e32 v178, v178
	v_exp_f32_e32 v179, v179
	v_pk_add_f32 v[172:173], v[172:173], 1.0 op_sel_hi:[1,0]
	v_pk_add_f32 v[174:175], v[174:175], 1.0 op_sel_hi:[1,0]
	v_pk_add_f32 v[176:177], v[176:177], 1.0 op_sel_hi:[1,0]
	v_pk_add_f32 v[178:179], v[178:179], 1.0 op_sel_hi:[1,0]
	v_rcp_f32_e32 v172, v172
	v_rcp_f32_e32 v173, v173
	v_rcp_f32_e32 v174, v174
	v_rcp_f32_e32 v175, v175
	v_rcp_f32_e32 v176, v176
	v_rcp_f32_e32 v177, v177
	v_rcp_f32_e32 v178, v178
	v_rcp_f32_e32 v179, v179
	v_pk_fma_f32 v[172:173], v[172:173], v[220:221], v[134:135]
	v_pk_fma_f32 v[174:175], v[174:175], v[222:223], v[136:137]
	v_pk_fma_f32 v[176:177], v[176:177], v[224:225], v[130:131]
	v_pk_fma_f32 v[178:179], v[178:179], v[226:227], v[132:133]
	v_max_f32_e32 v173, 0xda24260, v173
	v_max_f32_e32 v172, 0xda24260, v172
	v_max_f32_e32 v175, 0xda24260, v175
	v_max_f32_e32 v174, 0xda24260, v174
	v_max_f32_e32 v177, 0xda24260, v177
	v_max_f32_e32 v176, 0xda24260, v176
	v_max_f32_e32 v179, 0xda24260, v179
	v_max_f32_e32 v178, 0xda24260, v178
	v_log_f32_e32 v172, v172
	v_log_f32_e32 v173, v173
	v_log_f32_e32 v174, v174
	v_log_f32_e32 v175, v175
	v_log_f32_e32 v176, v176
	v_log_f32_e32 v177, v177
	v_log_f32_e32 v178, v178
	v_log_f32_e32 v179, v179
	v_pk_mul_f32 v[172:173], v[172:173], s[26:27] op_sel_hi:[1,0]
	v_pk_mul_f32 v[174:175], v[174:175], s[26:27] op_sel_hi:[1,0]
	v_pk_mul_f32 v[176:177], v[176:177], s[26:27] op_sel_hi:[1,0]
	v_pk_mul_f32 v[178:179], v[178:179], s[26:27] op_sel_hi:[1,0]
	v_cvt_pk_bf16_f32 v180, v172, v173
	v_cvt_pk_bf16_f32 v181, v174, v175
	v_cvt_pk_bf16_f32 v182, v176, v177
	v_cvt_pk_bf16_f32 v183, v178, v179
	global_store_dwordx4 v[170:171], v[180:183], off offset:256
	v_add_u32_e32 v170, 32, v189
	v_mad_i64_i32 v[170:171], s[2:3], v170, s17, v[166:167]
	v_lshl_add_u64 v[170:171], v[170:171], 0, v[168:169]
	v_pk_mul_f32 v[172:173], v[102:103], s[24:25] op_sel_hi:[1,0]
	v_pk_mul_f32 v[174:175], v[104:105], s[24:25] op_sel_hi:[1,0]
	v_pk_mul_f32 v[176:177], v[94:95], s[24:25] op_sel_hi:[1,0]
	v_pk_mul_f32 v[178:179], v[96:97], s[24:25] op_sel_hi:[1,0]
	v_exp_f32_e32 v172, v172
	v_exp_f32_e32 v173, v173
	v_exp_f32_e32 v174, v174
	v_exp_f32_e32 v175, v175
	v_exp_f32_e32 v176, v176
	v_exp_f32_e32 v177, v177
	v_exp_f32_e32 v178, v178
	v_exp_f32_e32 v179, v179
	v_pk_add_f32 v[172:173], v[172:173], 1.0 op_sel_hi:[1,0]
	v_pk_add_f32 v[174:175], v[174:175], 1.0 op_sel_hi:[1,0]
	v_pk_add_f32 v[176:177], v[176:177], 1.0 op_sel_hi:[1,0]
	v_pk_add_f32 v[178:179], v[178:179], 1.0 op_sel_hi:[1,0]
	v_rcp_f32_e32 v172, v172
	v_rcp_f32_e32 v173, v173
	v_rcp_f32_e32 v174, v174
	v_rcp_f32_e32 v175, v175
	v_rcp_f32_e32 v176, v176
	v_rcp_f32_e32 v177, v177
	v_rcp_f32_e32 v178, v178
	v_rcp_f32_e32 v179, v179
	v_pk_fma_f32 v[172:173], v[172:173], v[212:213], v[142:143]
	v_pk_fma_f32 v[174:175], v[174:175], v[214:215], v[144:145]
	v_pk_fma_f32 v[176:177], v[176:177], v[216:217], v[138:139]
	v_pk_fma_f32 v[178:179], v[178:179], v[218:219], v[140:141]
	v_max_f32_e32 v173, 0xda24260, v173
	v_max_f32_e32 v172, 0xda24260, v172
	v_max_f32_e32 v175, 0xda24260, v175
	v_max_f32_e32 v174, 0xda24260, v174
	v_max_f32_e32 v177, 0xda24260, v177
	v_max_f32_e32 v176, 0xda24260, v176
	v_max_f32_e32 v179, 0xda24260, v179
	v_max_f32_e32 v178, 0xda24260, v178
	v_log_f32_e32 v172, v172
	v_log_f32_e32 v173, v173
	v_log_f32_e32 v174, v174
	v_log_f32_e32 v175, v175
	v_log_f32_e32 v176, v176
	v_log_f32_e32 v177, v177
	v_log_f32_e32 v178, v178
	v_log_f32_e32 v179, v179
	v_pk_mul_f32 v[172:173], v[172:173], s[26:27] op_sel_hi:[1,0]
	v_pk_mul_f32 v[174:175], v[174:175], s[26:27] op_sel_hi:[1,0]
	v_pk_mul_f32 v[176:177], v[176:177], s[26:27] op_sel_hi:[1,0]
	v_pk_mul_f32 v[178:179], v[178:179], s[26:27] op_sel_hi:[1,0]
	v_cvt_pk_bf16_f32 v180, v172, v173
	v_cvt_pk_bf16_f32 v181, v174, v175
	v_cvt_pk_bf16_f32 v182, v176, v177
	v_cvt_pk_bf16_f32 v183, v178, v179
	global_store_dwordx4 v[170:171], v[180:183], off
	v_pk_mul_f32 v[172:173], v[82:83], s[24:25] op_sel_hi:[1,0]
	v_pk_mul_f32 v[174:175], v[84:85], s[24:25] op_sel_hi:[1,0]
	v_pk_mul_f32 v[176:177], v[74:75], s[24:25] op_sel_hi:[1,0]
	v_pk_mul_f32 v[178:179], v[76:77], s[24:25] op_sel_hi:[1,0]
	v_exp_f32_e32 v172, v172
	v_exp_f32_e32 v173, v173
	v_exp_f32_e32 v174, v174
	v_exp_f32_e32 v175, v175
	v_exp_f32_e32 v176, v176
	v_exp_f32_e32 v177, v177
	v_exp_f32_e32 v178, v178
	v_exp_f32_e32 v179, v179
	v_pk_add_f32 v[172:173], v[172:173], 1.0 op_sel_hi:[1,0]
	v_pk_add_f32 v[174:175], v[174:175], 1.0 op_sel_hi:[1,0]
	v_pk_add_f32 v[176:177], v[176:177], 1.0 op_sel_hi:[1,0]
	v_pk_add_f32 v[178:179], v[178:179], 1.0 op_sel_hi:[1,0]
	v_rcp_f32_e32 v172, v172
	v_rcp_f32_e32 v173, v173
	v_rcp_f32_e32 v174, v174
	v_rcp_f32_e32 v175, v175
	v_rcp_f32_e32 v176, v176
	v_rcp_f32_e32 v177, v177
	v_rcp_f32_e32 v178, v178
	v_rcp_f32_e32 v179, v179
	v_pk_fma_f32 v[172:173], v[172:173], v[220:221], v[134:135]
	v_pk_fma_f32 v[174:175], v[174:175], v[222:223], v[136:137]
	v_pk_fma_f32 v[176:177], v[176:177], v[224:225], v[130:131]
	v_pk_fma_f32 v[178:179], v[178:179], v[226:227], v[132:133]
	v_max_f32_e32 v173, 0xda24260, v173
	v_max_f32_e32 v172, 0xda24260, v172
	v_max_f32_e32 v175, 0xda24260, v175
	v_max_f32_e32 v174, 0xda24260, v174
	v_max_f32_e32 v177, 0xda24260, v177
	v_max_f32_e32 v176, 0xda24260, v176
	v_max_f32_e32 v179, 0xda24260, v179
	v_max_f32_e32 v178, 0xda24260, v178
	v_log_f32_e32 v172, v172
	v_log_f32_e32 v173, v173
	v_log_f32_e32 v174, v174
	v_log_f32_e32 v175, v175
	v_log_f32_e32 v176, v176
	v_log_f32_e32 v177, v177
	v_log_f32_e32 v178, v178
	v_log_f32_e32 v179, v179
	v_pk_mul_f32 v[172:173], v[172:173], s[26:27] op_sel_hi:[1,0]
	v_pk_mul_f32 v[174:175], v[174:175], s[26:27] op_sel_hi:[1,0]
	v_pk_mul_f32 v[176:177], v[176:177], s[26:27] op_sel_hi:[1,0]
	v_pk_mul_f32 v[178:179], v[178:179], s[26:27] op_sel_hi:[1,0]
	v_cvt_pk_bf16_f32 v180, v172, v173
	v_cvt_pk_bf16_f32 v181, v174, v175
	v_cvt_pk_bf16_f32 v182, v176, v177
	v_cvt_pk_bf16_f32 v183, v178, v179
	global_store_dwordx4 v[170:171], v[180:183], off offset:256
	v_add_u32_e32 v170, 48, v189
	v_mad_i64_i32 v[170:171], s[2:3], v170, s17, v[166:167]
	v_lshl_add_u64 v[170:171], v[170:171], 0, v[168:169]
	v_pk_mul_f32 v[172:173], v[86:87], s[24:25] op_sel_hi:[1,0]
	v_pk_mul_f32 v[174:175], v[88:89], s[24:25] op_sel_hi:[1,0]
	v_pk_mul_f32 v[176:177], v[78:79], s[24:25] op_sel_hi:[1,0]
	v_pk_mul_f32 v[178:179], v[80:81], s[24:25] op_sel_hi:[1,0]
	v_exp_f32_e32 v172, v172
	v_exp_f32_e32 v173, v173
	v_exp_f32_e32 v174, v174
	v_exp_f32_e32 v175, v175
	v_exp_f32_e32 v176, v176
	v_exp_f32_e32 v177, v177
	v_exp_f32_e32 v178, v178
	v_exp_f32_e32 v179, v179
	v_pk_add_f32 v[172:173], v[172:173], 1.0 op_sel_hi:[1,0]
	v_pk_add_f32 v[174:175], v[174:175], 1.0 op_sel_hi:[1,0]
	v_pk_add_f32 v[176:177], v[176:177], 1.0 op_sel_hi:[1,0]
	v_pk_add_f32 v[178:179], v[178:179], 1.0 op_sel_hi:[1,0]
	v_rcp_f32_e32 v172, v172
	v_rcp_f32_e32 v173, v173
	v_rcp_f32_e32 v174, v174
	v_rcp_f32_e32 v175, v175
	v_rcp_f32_e32 v176, v176
	v_rcp_f32_e32 v177, v177
	v_rcp_f32_e32 v178, v178
	v_rcp_f32_e32 v179, v179
	v_pk_fma_f32 v[172:173], v[172:173], v[212:213], v[142:143]
	v_pk_fma_f32 v[174:175], v[174:175], v[214:215], v[144:145]
	v_pk_fma_f32 v[176:177], v[176:177], v[216:217], v[138:139]
	v_pk_fma_f32 v[178:179], v[178:179], v[218:219], v[140:141]
	v_max_f32_e32 v173, 0xda24260, v173
	v_max_f32_e32 v172, 0xda24260, v172
	v_max_f32_e32 v175, 0xda24260, v175
	v_max_f32_e32 v174, 0xda24260, v174
	v_max_f32_e32 v177, 0xda24260, v177
	v_max_f32_e32 v176, 0xda24260, v176
	v_max_f32_e32 v179, 0xda24260, v179
	v_max_f32_e32 v178, 0xda24260, v178
	v_log_f32_e32 v172, v172
	v_log_f32_e32 v173, v173
	v_log_f32_e32 v174, v174
	v_log_f32_e32 v175, v175
	v_log_f32_e32 v176, v176
	v_log_f32_e32 v177, v177
	v_log_f32_e32 v178, v178
	v_log_f32_e32 v179, v179
	v_pk_mul_f32 v[172:173], v[172:173], s[26:27] op_sel_hi:[1,0]
	v_pk_mul_f32 v[174:175], v[174:175], s[26:27] op_sel_hi:[1,0]
	v_pk_mul_f32 v[176:177], v[176:177], s[26:27] op_sel_hi:[1,0]
	v_pk_mul_f32 v[178:179], v[178:179], s[26:27] op_sel_hi:[1,0]
	v_cvt_pk_bf16_f32 v180, v172, v173
	v_cvt_pk_bf16_f32 v181, v174, v175
	v_cvt_pk_bf16_f32 v182, v176, v177
	v_cvt_pk_bf16_f32 v183, v178, v179
	global_store_dwordx4 v[170:171], v[180:183], off
	v_pk_mul_f32 v[172:173], v[70:71], s[24:25] op_sel_hi:[1,0]
	v_pk_mul_f32 v[174:175], v[72:73], s[24:25] op_sel_hi:[1,0]
	v_pk_mul_f32 v[176:177], v[66:67], s[24:25] op_sel_hi:[1,0]
	v_pk_mul_f32 v[178:179], v[68:69], s[24:25] op_sel_hi:[1,0]
	v_exp_f32_e32 v172, v172
	v_exp_f32_e32 v173, v173
	v_exp_f32_e32 v174, v174
	v_exp_f32_e32 v175, v175
	v_exp_f32_e32 v176, v176
	v_exp_f32_e32 v177, v177
	v_exp_f32_e32 v178, v178
	v_exp_f32_e32 v179, v179
	v_pk_add_f32 v[172:173], v[172:173], 1.0 op_sel_hi:[1,0]
	v_pk_add_f32 v[174:175], v[174:175], 1.0 op_sel_hi:[1,0]
	v_pk_add_f32 v[176:177], v[176:177], 1.0 op_sel_hi:[1,0]
	v_pk_add_f32 v[178:179], v[178:179], 1.0 op_sel_hi:[1,0]
	v_rcp_f32_e32 v172, v172
	v_rcp_f32_e32 v173, v173
	v_rcp_f32_e32 v174, v174
	v_rcp_f32_e32 v175, v175
	v_rcp_f32_e32 v176, v176
	v_rcp_f32_e32 v177, v177
	v_rcp_f32_e32 v178, v178
	v_rcp_f32_e32 v179, v179
	v_pk_fma_f32 v[172:173], v[172:173], v[220:221], v[134:135]
	v_pk_fma_f32 v[174:175], v[174:175], v[222:223], v[136:137]
	v_pk_fma_f32 v[176:177], v[176:177], v[224:225], v[130:131]
	v_pk_fma_f32 v[178:179], v[178:179], v[226:227], v[132:133]
	v_max_f32_e32 v173, 0xda24260, v173
	v_max_f32_e32 v172, 0xda24260, v172
	v_max_f32_e32 v175, 0xda24260, v175
	v_max_f32_e32 v174, 0xda24260, v174
	v_max_f32_e32 v177, 0xda24260, v177
	v_max_f32_e32 v176, 0xda24260, v176
	v_max_f32_e32 v179, 0xda24260, v179
	v_max_f32_e32 v178, 0xda24260, v178
	v_log_f32_e32 v172, v172
	v_log_f32_e32 v173, v173
	v_log_f32_e32 v174, v174
	v_log_f32_e32 v175, v175
	v_log_f32_e32 v176, v176
	v_log_f32_e32 v177, v177
	v_log_f32_e32 v178, v178
	v_log_f32_e32 v179, v179
	v_pk_mul_f32 v[172:173], v[172:173], s[26:27] op_sel_hi:[1,0]
	v_pk_mul_f32 v[174:175], v[174:175], s[26:27] op_sel_hi:[1,0]
	v_pk_mul_f32 v[176:177], v[176:177], s[26:27] op_sel_hi:[1,0]
	v_pk_mul_f32 v[178:179], v[178:179], s[26:27] op_sel_hi:[1,0]
	v_cvt_pk_bf16_f32 v180, v172, v173
	v_cvt_pk_bf16_f32 v181, v174, v175
	v_cvt_pk_bf16_f32 v182, v176, v177
	v_cvt_pk_bf16_f32 v183, v178, v179
	global_store_dwordx4 v[170:171], v[180:183], off offset:256
	v_add_u32_e32 v170, 128, v189
	v_mad_i64_i32 v[170:171], s[2:3], v170, s17, v[166:167]
	v_lshl_add_u64 v[170:171], v[170:171], 0, v[168:169]
	v_pk_mul_f32 v[172:173], v[60:61], s[24:25] op_sel_hi:[1,0]
	v_pk_mul_f32 v[174:175], v[62:63], s[24:25] op_sel_hi:[1,0]
	v_pk_mul_f32 v[176:177], v[56:57], s[24:25] op_sel_hi:[1,0]
	v_pk_mul_f32 v[178:179], v[58:59], s[24:25] op_sel_hi:[1,0]
	v_exp_f32_e32 v172, v172
	v_exp_f32_e32 v173, v173
	v_exp_f32_e32 v174, v174
	v_exp_f32_e32 v175, v175
	v_exp_f32_e32 v176, v176
	v_exp_f32_e32 v177, v177
	v_exp_f32_e32 v178, v178
	v_exp_f32_e32 v179, v179
	v_pk_add_f32 v[172:173], v[172:173], 1.0 op_sel_hi:[1,0]
	v_pk_add_f32 v[174:175], v[174:175], 1.0 op_sel_hi:[1,0]
	v_pk_add_f32 v[176:177], v[176:177], 1.0 op_sel_hi:[1,0]
	v_pk_add_f32 v[178:179], v[178:179], 1.0 op_sel_hi:[1,0]
	v_rcp_f32_e32 v172, v172
	v_rcp_f32_e32 v173, v173
	v_rcp_f32_e32 v174, v174
	v_rcp_f32_e32 v175, v175
	v_rcp_f32_e32 v176, v176
	v_rcp_f32_e32 v177, v177
	v_rcp_f32_e32 v178, v178
	v_rcp_f32_e32 v179, v179
	v_pk_fma_f32 v[172:173], v[172:173], v[212:213], v[142:143]
	v_pk_fma_f32 v[174:175], v[174:175], v[214:215], v[144:145]
	v_pk_fma_f32 v[176:177], v[176:177], v[216:217], v[138:139]
	v_pk_fma_f32 v[178:179], v[178:179], v[218:219], v[140:141]
	v_max_f32_e32 v173, 0xda24260, v173
	v_max_f32_e32 v172, 0xda24260, v172
	v_max_f32_e32 v175, 0xda24260, v175
	v_max_f32_e32 v174, 0xda24260, v174
	v_max_f32_e32 v177, 0xda24260, v177
	v_max_f32_e32 v176, 0xda24260, v176
	v_max_f32_e32 v179, 0xda24260, v179
	v_max_f32_e32 v178, 0xda24260, v178
	v_log_f32_e32 v172, v172
	v_log_f32_e32 v173, v173
	v_log_f32_e32 v174, v174
	v_log_f32_e32 v175, v175
	v_log_f32_e32 v176, v176
	v_log_f32_e32 v177, v177
	v_log_f32_e32 v178, v178
	v_log_f32_e32 v179, v179
	v_pk_mul_f32 v[172:173], v[172:173], s[26:27] op_sel_hi:[1,0]
	v_pk_mul_f32 v[174:175], v[174:175], s[26:27] op_sel_hi:[1,0]
	v_pk_mul_f32 v[176:177], v[176:177], s[26:27] op_sel_hi:[1,0]
	v_pk_mul_f32 v[178:179], v[178:179], s[26:27] op_sel_hi:[1,0]
	v_cvt_pk_bf16_f32 v180, v172, v173
	v_cvt_pk_bf16_f32 v181, v174, v175
	v_cvt_pk_bf16_f32 v182, v176, v177
	v_cvt_pk_bf16_f32 v183, v178, v179
	global_store_dwordx4 v[170:171], v[180:183], off
	v_pk_mul_f32 v[172:173], v[48:49], s[24:25] op_sel_hi:[1,0]
	v_pk_mul_f32 v[174:175], v[50:51], s[24:25] op_sel_hi:[1,0]
	v_pk_mul_f32 v[176:177], v[40:41], s[24:25] op_sel_hi:[1,0]
	v_pk_mul_f32 v[178:179], v[42:43], s[24:25] op_sel_hi:[1,0]
	v_exp_f32_e32 v172, v172
	v_exp_f32_e32 v173, v173
	v_exp_f32_e32 v174, v174
	v_exp_f32_e32 v175, v175
	v_exp_f32_e32 v176, v176
	v_exp_f32_e32 v177, v177
	v_exp_f32_e32 v178, v178
	v_exp_f32_e32 v179, v179
	v_pk_add_f32 v[172:173], v[172:173], 1.0 op_sel_hi:[1,0]
	v_pk_add_f32 v[174:175], v[174:175], 1.0 op_sel_hi:[1,0]
	v_pk_add_f32 v[176:177], v[176:177], 1.0 op_sel_hi:[1,0]
	v_pk_add_f32 v[178:179], v[178:179], 1.0 op_sel_hi:[1,0]
	v_rcp_f32_e32 v172, v172
	v_rcp_f32_e32 v173, v173
	v_rcp_f32_e32 v174, v174
	v_rcp_f32_e32 v175, v175
	v_rcp_f32_e32 v176, v176
	v_rcp_f32_e32 v177, v177
	v_rcp_f32_e32 v178, v178
	v_rcp_f32_e32 v179, v179
	v_pk_fma_f32 v[172:173], v[172:173], v[220:221], v[134:135]
	v_pk_fma_f32 v[174:175], v[174:175], v[222:223], v[136:137]
	v_pk_fma_f32 v[176:177], v[176:177], v[224:225], v[130:131]
	v_pk_fma_f32 v[178:179], v[178:179], v[226:227], v[132:133]
	v_max_f32_e32 v173, 0xda24260, v173
	v_max_f32_e32 v172, 0xda24260, v172
	v_max_f32_e32 v175, 0xda24260, v175
	v_max_f32_e32 v174, 0xda24260, v174
	v_max_f32_e32 v177, 0xda24260, v177
	v_max_f32_e32 v176, 0xda24260, v176
	v_max_f32_e32 v179, 0xda24260, v179
	v_max_f32_e32 v178, 0xda24260, v178
	v_log_f32_e32 v172, v172
	v_log_f32_e32 v173, v173
	v_log_f32_e32 v174, v174
	v_log_f32_e32 v175, v175
	v_log_f32_e32 v176, v176
	v_log_f32_e32 v177, v177
	v_log_f32_e32 v178, v178
	v_log_f32_e32 v179, v179
	v_pk_mul_f32 v[172:173], v[172:173], s[26:27] op_sel_hi:[1,0]
	v_pk_mul_f32 v[174:175], v[174:175], s[26:27] op_sel_hi:[1,0]
	v_pk_mul_f32 v[176:177], v[176:177], s[26:27] op_sel_hi:[1,0]
	v_pk_mul_f32 v[178:179], v[178:179], s[26:27] op_sel_hi:[1,0]
	v_cvt_pk_bf16_f32 v180, v172, v173
	v_cvt_pk_bf16_f32 v181, v174, v175
	v_cvt_pk_bf16_f32 v182, v176, v177
	v_cvt_pk_bf16_f32 v183, v178, v179
	global_store_dwordx4 v[170:171], v[180:183], off offset:256
	v_add_u32_e32 v170, 144, v189
	v_mad_i64_i32 v[170:171], s[2:3], v170, s17, v[166:167]
	v_lshl_add_u64 v[170:171], v[170:171], 0, v[168:169]
	v_pk_mul_f32 v[172:173], v[52:53], s[24:25] op_sel_hi:[1,0]
	v_pk_mul_f32 v[174:175], v[54:55], s[24:25] op_sel_hi:[1,0]
	v_pk_mul_f32 v[176:177], v[44:45], s[24:25] op_sel_hi:[1,0]
	v_pk_mul_f32 v[178:179], v[46:47], s[24:25] op_sel_hi:[1,0]
	v_exp_f32_e32 v172, v172
	v_exp_f32_e32 v173, v173
	v_exp_f32_e32 v174, v174
	v_exp_f32_e32 v175, v175
	v_exp_f32_e32 v176, v176
	v_exp_f32_e32 v177, v177
	v_exp_f32_e32 v178, v178
	v_exp_f32_e32 v179, v179
	v_pk_add_f32 v[172:173], v[172:173], 1.0 op_sel_hi:[1,0]
	v_pk_add_f32 v[174:175], v[174:175], 1.0 op_sel_hi:[1,0]
	v_pk_add_f32 v[176:177], v[176:177], 1.0 op_sel_hi:[1,0]
	v_pk_add_f32 v[178:179], v[178:179], 1.0 op_sel_hi:[1,0]
	v_rcp_f32_e32 v172, v172
	v_rcp_f32_e32 v173, v173
	v_rcp_f32_e32 v174, v174
	v_rcp_f32_e32 v175, v175
	v_rcp_f32_e32 v176, v176
	v_rcp_f32_e32 v177, v177
	v_rcp_f32_e32 v178, v178
	v_rcp_f32_e32 v179, v179
	v_pk_fma_f32 v[172:173], v[172:173], v[212:213], v[142:143]
	v_pk_fma_f32 v[174:175], v[174:175], v[214:215], v[144:145]
	v_pk_fma_f32 v[176:177], v[176:177], v[216:217], v[138:139]
	v_pk_fma_f32 v[178:179], v[178:179], v[218:219], v[140:141]
	v_max_f32_e32 v173, 0xda24260, v173
	v_max_f32_e32 v172, 0xda24260, v172
	v_max_f32_e32 v175, 0xda24260, v175
	v_max_f32_e32 v174, 0xda24260, v174
	v_max_f32_e32 v177, 0xda24260, v177
	v_max_f32_e32 v176, 0xda24260, v176
	v_max_f32_e32 v179, 0xda24260, v179
	v_max_f32_e32 v178, 0xda24260, v178
	v_log_f32_e32 v172, v172
	v_log_f32_e32 v173, v173
	v_log_f32_e32 v174, v174
	v_log_f32_e32 v175, v175
	v_log_f32_e32 v176, v176
	v_log_f32_e32 v177, v177
	v_log_f32_e32 v178, v178
	v_log_f32_e32 v179, v179
	v_pk_mul_f32 v[172:173], v[172:173], s[26:27] op_sel_hi:[1,0]
	v_pk_mul_f32 v[174:175], v[174:175], s[26:27] op_sel_hi:[1,0]
	v_pk_mul_f32 v[176:177], v[176:177], s[26:27] op_sel_hi:[1,0]
	v_pk_mul_f32 v[178:179], v[178:179], s[26:27] op_sel_hi:[1,0]
	v_cvt_pk_bf16_f32 v180, v172, v173
	v_cvt_pk_bf16_f32 v181, v174, v175
	v_cvt_pk_bf16_f32 v182, v176, v177
	v_cvt_pk_bf16_f32 v183, v178, v179
	global_store_dwordx4 v[170:171], v[180:183], off
	v_pk_mul_f32 v[172:173], v[32:33], s[24:25] op_sel_hi:[1,0]
	v_pk_mul_f32 v[174:175], v[34:35], s[24:25] op_sel_hi:[1,0]
	v_pk_mul_f32 v[176:177], v[24:25], s[24:25] op_sel_hi:[1,0]
	v_pk_mul_f32 v[178:179], v[26:27], s[24:25] op_sel_hi:[1,0]
	v_exp_f32_e32 v172, v172
	v_exp_f32_e32 v173, v173
	v_exp_f32_e32 v174, v174
	v_exp_f32_e32 v175, v175
	v_exp_f32_e32 v176, v176
	v_exp_f32_e32 v177, v177
	v_exp_f32_e32 v178, v178
	v_exp_f32_e32 v179, v179
	v_pk_add_f32 v[172:173], v[172:173], 1.0 op_sel_hi:[1,0]
	v_pk_add_f32 v[174:175], v[174:175], 1.0 op_sel_hi:[1,0]
	v_pk_add_f32 v[176:177], v[176:177], 1.0 op_sel_hi:[1,0]
	v_pk_add_f32 v[178:179], v[178:179], 1.0 op_sel_hi:[1,0]
	v_rcp_f32_e32 v172, v172
	v_rcp_f32_e32 v173, v173
	v_rcp_f32_e32 v174, v174
	v_rcp_f32_e32 v175, v175
	v_rcp_f32_e32 v176, v176
	v_rcp_f32_e32 v177, v177
	v_rcp_f32_e32 v178, v178
	v_rcp_f32_e32 v179, v179
	v_pk_fma_f32 v[172:173], v[172:173], v[220:221], v[134:135]
	v_pk_fma_f32 v[174:175], v[174:175], v[222:223], v[136:137]
	v_pk_fma_f32 v[176:177], v[176:177], v[224:225], v[130:131]
	v_pk_fma_f32 v[178:179], v[178:179], v[226:227], v[132:133]
	v_max_f32_e32 v173, 0xda24260, v173
	v_max_f32_e32 v172, 0xda24260, v172
	v_max_f32_e32 v175, 0xda24260, v175
	v_max_f32_e32 v174, 0xda24260, v174
	v_max_f32_e32 v177, 0xda24260, v177
	v_max_f32_e32 v176, 0xda24260, v176
	v_max_f32_e32 v179, 0xda24260, v179
	v_max_f32_e32 v178, 0xda24260, v178
	v_log_f32_e32 v172, v172
	v_log_f32_e32 v173, v173
	v_log_f32_e32 v174, v174
	v_log_f32_e32 v175, v175
	v_log_f32_e32 v176, v176
	v_log_f32_e32 v177, v177
	v_log_f32_e32 v178, v178
	v_log_f32_e32 v179, v179
	v_pk_mul_f32 v[172:173], v[172:173], s[26:27] op_sel_hi:[1,0]
	v_pk_mul_f32 v[174:175], v[174:175], s[26:27] op_sel_hi:[1,0]
	v_pk_mul_f32 v[176:177], v[176:177], s[26:27] op_sel_hi:[1,0]
	v_pk_mul_f32 v[178:179], v[178:179], s[26:27] op_sel_hi:[1,0]
	v_cvt_pk_bf16_f32 v180, v172, v173
	v_cvt_pk_bf16_f32 v181, v174, v175
	v_cvt_pk_bf16_f32 v182, v176, v177
	v_cvt_pk_bf16_f32 v183, v178, v179
	global_store_dwordx4 v[170:171], v[180:183], off offset:256
	v_add_u32_e32 v170, 160, v189
	v_mad_i64_i32 v[170:171], s[2:3], v170, s17, v[166:167]
	v_lshl_add_u64 v[170:171], v[170:171], 0, v[168:169]
	v_pk_mul_f32 v[172:173], v[36:37], s[24:25] op_sel_hi:[1,0]
	v_pk_mul_f32 v[174:175], v[38:39], s[24:25] op_sel_hi:[1,0]
	v_pk_mul_f32 v[176:177], v[28:29], s[24:25] op_sel_hi:[1,0]
	v_pk_mul_f32 v[178:179], v[30:31], s[24:25] op_sel_hi:[1,0]
	v_exp_f32_e32 v172, v172
	v_exp_f32_e32 v173, v173
	v_exp_f32_e32 v174, v174
	v_exp_f32_e32 v175, v175
	v_exp_f32_e32 v176, v176
	v_exp_f32_e32 v177, v177
	v_exp_f32_e32 v178, v178
	v_exp_f32_e32 v179, v179
	v_pk_add_f32 v[172:173], v[172:173], 1.0 op_sel_hi:[1,0]
	v_pk_add_f32 v[174:175], v[174:175], 1.0 op_sel_hi:[1,0]
	v_pk_add_f32 v[176:177], v[176:177], 1.0 op_sel_hi:[1,0]
	v_pk_add_f32 v[178:179], v[178:179], 1.0 op_sel_hi:[1,0]
	v_rcp_f32_e32 v172, v172
	v_rcp_f32_e32 v173, v173
	v_rcp_f32_e32 v174, v174
	v_rcp_f32_e32 v175, v175
	v_rcp_f32_e32 v176, v176
	v_rcp_f32_e32 v177, v177
	v_rcp_f32_e32 v178, v178
	v_rcp_f32_e32 v179, v179
	v_pk_fma_f32 v[172:173], v[172:173], v[212:213], v[142:143]
	v_pk_fma_f32 v[174:175], v[174:175], v[214:215], v[144:145]
	v_pk_fma_f32 v[176:177], v[176:177], v[216:217], v[138:139]
	v_pk_fma_f32 v[178:179], v[178:179], v[218:219], v[140:141]
	v_max_f32_e32 v173, 0xda24260, v173
	v_max_f32_e32 v172, 0xda24260, v172
	v_max_f32_e32 v175, 0xda24260, v175
	v_max_f32_e32 v174, 0xda24260, v174
	v_max_f32_e32 v177, 0xda24260, v177
	v_max_f32_e32 v176, 0xda24260, v176
	v_max_f32_e32 v179, 0xda24260, v179
	v_max_f32_e32 v178, 0xda24260, v178
	v_log_f32_e32 v172, v172
	v_log_f32_e32 v173, v173
	v_log_f32_e32 v174, v174
	v_log_f32_e32 v175, v175
	v_log_f32_e32 v176, v176
	v_log_f32_e32 v177, v177
	v_log_f32_e32 v178, v178
	v_log_f32_e32 v179, v179
	v_pk_mul_f32 v[172:173], v[172:173], s[26:27] op_sel_hi:[1,0]
	v_pk_mul_f32 v[174:175], v[174:175], s[26:27] op_sel_hi:[1,0]
	v_pk_mul_f32 v[176:177], v[176:177], s[26:27] op_sel_hi:[1,0]
	v_pk_mul_f32 v[178:179], v[178:179], s[26:27] op_sel_hi:[1,0]
	v_cvt_pk_bf16_f32 v180, v172, v173
	v_cvt_pk_bf16_f32 v181, v174, v175
	v_cvt_pk_bf16_f32 v182, v176, v177
	v_cvt_pk_bf16_f32 v183, v178, v179
	global_store_dwordx4 v[170:171], v[180:183], off
	v_pk_mul_f32 v[172:173], v[16:17], s[24:25] op_sel_hi:[1,0]
	v_pk_mul_f32 v[174:175], v[18:19], s[24:25] op_sel_hi:[1,0]
	v_pk_mul_f32 v[176:177], v[8:9], s[24:25] op_sel_hi:[1,0]
	v_pk_mul_f32 v[178:179], v[10:11], s[24:25] op_sel_hi:[1,0]
	v_exp_f32_e32 v172, v172
	v_exp_f32_e32 v173, v173
	v_exp_f32_e32 v174, v174
	v_exp_f32_e32 v175, v175
	v_exp_f32_e32 v176, v176
	v_exp_f32_e32 v177, v177
	v_exp_f32_e32 v178, v178
	v_exp_f32_e32 v179, v179
	v_pk_add_f32 v[172:173], v[172:173], 1.0 op_sel_hi:[1,0]
	v_pk_add_f32 v[174:175], v[174:175], 1.0 op_sel_hi:[1,0]
	v_pk_add_f32 v[176:177], v[176:177], 1.0 op_sel_hi:[1,0]
	v_pk_add_f32 v[178:179], v[178:179], 1.0 op_sel_hi:[1,0]
	v_rcp_f32_e32 v172, v172
	v_rcp_f32_e32 v173, v173
	v_rcp_f32_e32 v174, v174
	v_rcp_f32_e32 v175, v175
	v_rcp_f32_e32 v176, v176
	v_rcp_f32_e32 v177, v177
	v_rcp_f32_e32 v178, v178
	v_rcp_f32_e32 v179, v179
	v_pk_fma_f32 v[172:173], v[172:173], v[220:221], v[134:135]
	v_pk_fma_f32 v[174:175], v[174:175], v[222:223], v[136:137]
	v_pk_fma_f32 v[176:177], v[176:177], v[224:225], v[130:131]
	v_pk_fma_f32 v[178:179], v[178:179], v[226:227], v[132:133]
	v_max_f32_e32 v173, 0xda24260, v173
	v_max_f32_e32 v172, 0xda24260, v172
	v_max_f32_e32 v175, 0xda24260, v175
	v_max_f32_e32 v174, 0xda24260, v174
	v_max_f32_e32 v177, 0xda24260, v177
	v_max_f32_e32 v176, 0xda24260, v176
	v_max_f32_e32 v179, 0xda24260, v179
	v_max_f32_e32 v178, 0xda24260, v178
	v_log_f32_e32 v172, v172
	v_log_f32_e32 v173, v173
	v_log_f32_e32 v174, v174
	v_log_f32_e32 v175, v175
	v_log_f32_e32 v176, v176
	v_log_f32_e32 v177, v177
	v_log_f32_e32 v178, v178
	v_log_f32_e32 v179, v179
	v_pk_mul_f32 v[172:173], v[172:173], s[26:27] op_sel_hi:[1,0]
	v_pk_mul_f32 v[174:175], v[174:175], s[26:27] op_sel_hi:[1,0]
	v_pk_mul_f32 v[176:177], v[176:177], s[26:27] op_sel_hi:[1,0]
	v_pk_mul_f32 v[178:179], v[178:179], s[26:27] op_sel_hi:[1,0]
	v_cvt_pk_bf16_f32 v180, v172, v173
	v_cvt_pk_bf16_f32 v181, v174, v175
	v_cvt_pk_bf16_f32 v182, v176, v177
	v_cvt_pk_bf16_f32 v183, v178, v179
	global_store_dwordx4 v[170:171], v[180:183], off offset:256
	v_add_u32_e32 v162, 176, v189
	v_mad_i64_i32 v[162:163], s[2:3], v162, s17, v[166:167]
	v_lshl_add_u64 v[162:163], v[162:163], 0, v[168:169]
	v_pk_mul_f32 v[172:173], v[20:21], s[24:25] op_sel_hi:[1,0]
	v_pk_mul_f32 v[174:175], v[22:23], s[24:25] op_sel_hi:[1,0]
	v_pk_mul_f32 v[176:177], v[12:13], s[24:25] op_sel_hi:[1,0]
	v_pk_mul_f32 v[178:179], v[14:15], s[24:25] op_sel_hi:[1,0]
	v_exp_f32_e32 v172, v172
	v_exp_f32_e32 v173, v173
	v_exp_f32_e32 v174, v174
	v_exp_f32_e32 v175, v175
	v_exp_f32_e32 v176, v176
	v_exp_f32_e32 v177, v177
	v_exp_f32_e32 v178, v178
	v_exp_f32_e32 v179, v179
	v_pk_add_f32 v[172:173], v[172:173], 1.0 op_sel_hi:[1,0]
	v_pk_add_f32 v[174:175], v[174:175], 1.0 op_sel_hi:[1,0]
	v_pk_add_f32 v[176:177], v[176:177], 1.0 op_sel_hi:[1,0]
	v_pk_add_f32 v[178:179], v[178:179], 1.0 op_sel_hi:[1,0]
	v_rcp_f32_e32 v172, v172
	v_rcp_f32_e32 v173, v173
	v_rcp_f32_e32 v174, v174
	v_rcp_f32_e32 v175, v175
	v_rcp_f32_e32 v176, v176
	v_rcp_f32_e32 v177, v177
	v_rcp_f32_e32 v178, v178
	v_rcp_f32_e32 v179, v179
	v_pk_fma_f32 v[172:173], v[172:173], v[212:213], v[142:143]
	v_pk_fma_f32 v[174:175], v[174:175], v[214:215], v[144:145]
	v_pk_fma_f32 v[176:177], v[176:177], v[216:217], v[138:139]
	v_pk_fma_f32 v[178:179], v[178:179], v[218:219], v[140:141]
	v_max_f32_e32 v173, 0xda24260, v173
	v_max_f32_e32 v172, 0xda24260, v172
	v_max_f32_e32 v175, 0xda24260, v175
	v_max_f32_e32 v174, 0xda24260, v174
	v_max_f32_e32 v177, 0xda24260, v177
	v_max_f32_e32 v176, 0xda24260, v176
	v_max_f32_e32 v179, 0xda24260, v179
	v_max_f32_e32 v178, 0xda24260, v178
	v_log_f32_e32 v172, v172
	v_log_f32_e32 v173, v173
	v_log_f32_e32 v174, v174
	v_log_f32_e32 v175, v175
	v_log_f32_e32 v176, v176
	v_log_f32_e32 v177, v177
	v_log_f32_e32 v178, v178
	v_log_f32_e32 v179, v179
	v_pk_mul_f32 v[172:173], v[172:173], s[26:27] op_sel_hi:[1,0]
	v_pk_mul_f32 v[174:175], v[174:175], s[26:27] op_sel_hi:[1,0]
	v_pk_mul_f32 v[176:177], v[176:177], s[26:27] op_sel_hi:[1,0]
	v_pk_mul_f32 v[178:179], v[178:179], s[26:27] op_sel_hi:[1,0]
	v_cvt_pk_bf16_f32 v180, v172, v173
	v_cvt_pk_bf16_f32 v181, v174, v175
	v_cvt_pk_bf16_f32 v182, v176, v177
	v_cvt_pk_bf16_f32 v183, v178, v179
	global_store_dwordx4 v[162:163], v[180:183], off
	v_pk_mul_f32 v[172:173], v[4:5], s[24:25] op_sel_hi:[1,0]
	v_pk_mul_f32 v[174:175], v[6:7], s[24:25] op_sel_hi:[1,0]
	v_pk_mul_f32 v[176:177], v[0:1], s[24:25] op_sel_hi:[1,0]
	v_pk_mul_f32 v[178:179], v[2:3], s[24:25] op_sel_hi:[1,0]
	v_exp_f32_e32 v172, v172
	v_exp_f32_e32 v173, v173
	v_exp_f32_e32 v174, v174
	v_exp_f32_e32 v175, v175
	v_exp_f32_e32 v176, v176
	v_exp_f32_e32 v177, v177
	v_exp_f32_e32 v178, v178
	v_exp_f32_e32 v179, v179
	v_pk_add_f32 v[172:173], v[172:173], 1.0 op_sel_hi:[1,0]
	v_pk_add_f32 v[174:175], v[174:175], 1.0 op_sel_hi:[1,0]
	v_pk_add_f32 v[176:177], v[176:177], 1.0 op_sel_hi:[1,0]
	v_pk_add_f32 v[178:179], v[178:179], 1.0 op_sel_hi:[1,0]
	v_rcp_f32_e32 v172, v172
	v_rcp_f32_e32 v173, v173
	v_rcp_f32_e32 v174, v174
	v_rcp_f32_e32 v175, v175
	v_rcp_f32_e32 v176, v176
	v_rcp_f32_e32 v177, v177
	v_rcp_f32_e32 v178, v178
	v_rcp_f32_e32 v179, v179
	v_pk_fma_f32 v[172:173], v[172:173], v[220:221], v[134:135]
	v_pk_fma_f32 v[174:175], v[174:175], v[222:223], v[136:137]
	v_pk_fma_f32 v[176:177], v[176:177], v[224:225], v[130:131]
	v_pk_fma_f32 v[178:179], v[178:179], v[226:227], v[132:133]
	v_max_f32_e32 v173, 0xda24260, v173
	v_max_f32_e32 v172, 0xda24260, v172
	v_max_f32_e32 v175, 0xda24260, v175
	v_max_f32_e32 v174, 0xda24260, v174
	v_max_f32_e32 v177, 0xda24260, v177
	v_max_f32_e32 v176, 0xda24260, v176
	v_max_f32_e32 v179, 0xda24260, v179
	v_max_f32_e32 v178, 0xda24260, v178
	v_log_f32_e32 v172, v172
	v_log_f32_e32 v173, v173
	v_log_f32_e32 v174, v174
	v_log_f32_e32 v175, v175
	v_log_f32_e32 v176, v176
	v_log_f32_e32 v177, v177
	v_log_f32_e32 v178, v178
	v_log_f32_e32 v179, v179
	v_pk_mul_f32 v[172:173], v[172:173], s[26:27] op_sel_hi:[1,0]
	v_pk_mul_f32 v[174:175], v[174:175], s[26:27] op_sel_hi:[1,0]
	v_pk_mul_f32 v[176:177], v[176:177], s[26:27] op_sel_hi:[1,0]
	v_pk_mul_f32 v[178:179], v[178:179], s[26:27] op_sel_hi:[1,0]
	v_cvt_pk_bf16_f32 v180, v172, v173
	v_cvt_pk_bf16_f32 v181, v174, v175
	v_cvt_pk_bf16_f32 v182, v176, v177
	v_cvt_pk_bf16_f32 v183, v178, v179
	v_mov_b32_e32 v130, v180
	v_mov_b32_e32 v131, v181
	v_mov_b32_e32 v132, v182
	v_mov_b32_e32 v133, v183
	s_branch .LBB0_328
